# P2 attention: counted lgkmcnt waits inside the QK MFMA runs, group-B bias table fill with 4 loads in flight instead of 4 round trips, group-A prologue wait leaves the tile DMAs in flight
# baseline (speedup 1.0000x reference)
; template <bool ISA>
; __device__ __forceinline__ void attn_unit(const Params& p, unsigned char* smem, int b, int hh, int blk) {
;     ...
;         int rs = 2 * blk - 4; rs = rs < 0 ? 0 : (rs > 119 ? 119 : rs);
;         nl = 9; tbase = rs * 64;
;     }
;     const int ntile = nl + 4;
;     const bf16_t* kbase; const bf16_t* vbase; int ldk;
;     if (ISA) { const int g = hh >> 2; kbase = p.ka + (size_t)(b * TT) * 128 + g * 64; ldk = 128; vbase = p.vta + (size_t)((b * 2 + g) * 64) * TT; }
;     else { kbase = p.kb + (size_t)(b * TT) * 512 + hh * 64; ldk = 512; vbase = p.vtb + (size_t)((b * 8 + hh) * 64) * TT; }
;     float* rpbl = (float*)(smem + 49152);
;     const float M2 = p.attm[ISA ? hh : 8 + hh], negM2 = -M2;
;     const int qt0 = ISA ? blk * 128 + wid * 32 : blk * 128 + wid * 16;
;     bf16x8 qf[NQ][2];
;     {
;         const bf16_t* qsrc = ISA ? p.qa : p.qb;
; #pragma unroll
;         for (int q = 0; q < NQ; ++q)
; #pragma unroll
;             for (int ks = 0; ks < 2; ++ks)
;                 qf[q][ks] = *(const bf16x8*)(qsrc + (size_t)(b * TT + qt0 + q * QSTR + l15) * 512 + hh * 64 + ks * 32 + gq * 8);
;     }
;     f32x4 osum[NQ]; f32x4 o[NQ][4];
; #pragma unroll
;     for (int q = 0; q < NQ; ++q) {
;         const float l0 = ISA ? __builtin_amdgcn_exp2f(p.sink[hh] * L2E - M2) : 0.f;
;         osum[q] = (f32x4){l0, l0, l0, l0};
; #pragma unroll
;         for (int df = 0; df < 4; ++df) o[q][df] = (f32x4){0.f, 0.f, 0.f, 0.f};
;     }
;     const int qcol = wid * 16 + l15;
;     int cs = wid * 16 - 8; cs = cs < 0 ? 0 : (cs > 32 ? 32 : cs);
;     int wstart = qcol - 8; wstart = wstart < 0 ? 0 : (wstart > 48 ? 48 : wstart);
;     NaConst nc;
; #pragma unroll
;     for (int j = 0; j < 4; ++j) {
;         const int kc = cs + (j >> 1) * 16 + gq * 4 + (j & 1) * 2;
;         nc.cm[j] = (((kc >= wstart) && (kc < wstart + 16)) ? 0xFFFFu : 0u) | (((kc + 1 >= wstart) && (kc + 1 < wstart + 16)) ? 0xFFFF0000u : 0u);
; __device__ void phase2(const Params& p, unsigned char* smem, unsigned* qw) {
;     ...
;             if (item >= 256) { if (++aq == 8) att_left = false; continue; }
;             if (item < 128) {
;                 const int u = item * 2 + sub;
;                 attn_unit<true>(p, sm, q >> 1, (q & 1) * 4 + (u & 3), u >> 2);
;             } else {
;                 const int j = item - 128;
;                 attn_unit<false>(p, sm, j >> 5, q, (j & 31) * 2 + sub);
.LBB0_377:
	s_or_b64 exec, exec, s[6:7]
	s_waitcnt lgkmcnt(0)
	s_barrier
	s_waitcnt vmcnt(0)
	ds_read_b32 v2, v118
	s_xor_b64 s[6:7], s[0:1], -1
	s_mov_b64 s[0:1], -1
	s_and_b64 vcc, exec, s[6:7]
	s_waitcnt lgkmcnt(0)
	v_readfirstlane_b32 s4, v2
	s_cbranch_vccz .LBB0_429
	s_cmpk_lt_i32 s4, 0x100
	s_cbranch_scc0 .LBB0_426
	s_cmpk_gt_i32 s4, 0x7f
	s_cbranch_scc0 .LBB0_401
	s_add_i32 s0, s4, 0xffffff80
	s_lshr_b32 s24, s0, 5
	s_lshl_b32 s76, s5, 6
	s_lshl_b32 s6, s24, 9
	s_lshl_b32 s0, s4, 1
	s_or_b32 s6, s6, s76
	s_and_b32 s0, s0, 62
	s_mulk_i32 s6, 0x2100
	s_mov_b32 s7, s77
	v_add_u32_e32 v21, s0, v1
	v_mov_b32_e32 v30, v0
	s_lshl_b64 s[6:7], s[6:7], 1
	v_readlane_b32 s9, v248, 26
	v_lshlrev_b32_e32 v101, 1, v21
	v_bfe_u32 v31, v30, 6, 2
	s_add_u32 s6, s9, s6
	v_readlane_b32 s9, v248, 28
	v_add_u32_e32 v19, -4, v101
	s_addc_u32 s7, s9, s7
	s_or_b32 s23, s5, 8
	v_lshlrev_b32_e32 v20, 4, v31
	v_min_i32_e32 v2, 0x77, v19
	s_mul_i32 s8, s24, 0x2100
	s_lshl_b32 s9, s23, 2
	v_lshl_or_b32 v100, v21, 7, v20
	v_lshlrev_b32_e32 v22, 6, v2
	v_mov_b32_e32 v4, s9
	v_add_u32_e32 v2, s8, v100
	s_lshl_b32 s10, s5, 7
	v_readlane_b32 s8, v248, 9
	v_and_b32_e32 v112, 15, v30
	v_readlane_b32 s9, v248, 10
	s_add_u32 s8, s8, s10
	v_or_b32_e32 v6, v2, v112
	s_addc_u32 s9, s9, 0
	v_and_b32_e32 v98, 48, v30
	v_lshl_add_u64 v[8:9], s[8:9], 0, v[98:99]
	v_ashrrev_i32_e32 v7, 31, v6
	v_readlane_b32 s8, v248, 20
	s_mul_i32 s0, s24, 0x420000
	s_mov_b32 s1, s77
	v_lshlrev_b64 v[2:3], 10, v[6:7]
	v_readlane_b32 s9, v248, 21
	v_lshl_add_u64 v[10:11], v[8:9], 0, v[2:3]
	s_nop 3
	global_load_dword v113, v4, s[8:9]
	s_nop 0
	global_load_dwordx4 v[2:5], v[10:11], off
	s_lshl_b64 s[0:1], s[0:1], 1
	v_readlane_b32 s8, v248, 7
	v_readlane_b32 s9, v248, 8
	s_add_u32 s0, s8, s0
	v_cmp_gt_i32_e32 vcc, 2, v21
	v_bfe_u32 v21, v30, 3, 3
	s_addc_u32 s1, s9, s1
	v_or_b32_e32 v21, v20, v21
	v_bfe_u32 v18, v30, 4, 2
	s_add_u32 s0, s0, s10
	v_or_b32_e32 v28, 8, v21
	s_addc_u32 s1, s1, 0
	v_cndmask_b32_e64 v102, v22, 0, vcc
	v_bitop3_b32 v24, v18, v30, 7 bitop3:0x78
	v_lshrrev_b32_e32 v22, 1, v28
	v_lshlrev_b32_e32 v98, 10, v21
	v_xor_b32_e32 v25, v22, v30
	v_lshl_add_u64 v[22:23], s[0:1], 0, v[98:99]
	v_lshlrev_b32_e32 v98, 4, v24
	v_lshl_add_u64 v[104:105], v[22:23], 0, v[98:99]
	v_lshlrev_b32_e32 v22, 10, v28
	v_mov_b32_e32 v23, v99
	v_lshlrev_b32_e32 v24, 4, v25
	v_or_b32_e32 v6, 64, v6
	v_readfirstlane_b32 s8, v31
	v_lshl_add_u64 v[22:23], s[0:1], 0, v[22:23]
	v_and_b32_e32 v24, 0x70, v24
	v_mov_b32_e32 v25, v99
	v_ashrrev_i32_e32 v7, 31, v6
	v_lshl_add_u64 v[106:107], v[22:23], 0, v[24:25]
	v_mov_b64_e32 v[22:23], s[6:7]
	s_movk_i32 s6, 0x4200
	s_lshl_b32 s25, s8, 11
	v_lshlrev_b64 v[6:7], 10, v[6:7]
	v_mad_u64_u32 v[26:27], s[0:1], v21, s6, v[22:23]
	v_mad_u64_u32 v[22:23], s[0:1], v28, s6, v[22:23]
	v_ashrrev_i32_e32 v103, 31, v102
	v_add_u32_e32 v21, s25, v114
	v_lshl_add_u64 v[14:15], v[8:9], 0, v[6:7]
	v_lshl_add_u64 v[108:109], v[26:27], 0, v[98:99]
	v_lshl_add_u64 v[110:111], v[22:23], 0, v[24:25]
	v_lshlrev_b64 v[22:23], 10, v[102:103]
	v_readfirstlane_b32 s0, v21
	v_add_u32_e32 v26, 0x400, v21
	global_load_dwordx4 v[6:9], v[10:11], off offset:64
	s_nop 0
	global_load_dwordx4 v[10:13], v[14:15], off
	s_nop 0
	global_load_dwordx4 v[14:17], v[14:15], off offset:64
	s_waitcnt lgkmcnt(0)
	s_barrier
; #define LAS __attribute__((address_space(3)))
; template <bool ISA>
; __device__ __forceinline__ void attn_unit(const Params& p, unsigned char* smem, int b, int hh, int blk) {
;     ...
;     const int qcol = wid * 16 + l15;
;     int cs = wid * 16 - 8; cs = cs < 0 ? 0 : (cs > 32 ? 32 : cs);
;     int wstart = qcol - 8; wstart = wstart < 0 ? 0 : (wstart > 48 ? 48 : wstart);
;     NaConst nc;
; #pragma unroll
;     for (int j = 0; j < 4; ++j) {
;         const int kc = cs + (j >> 1) * 16 + gq * 4 + (j & 1) * 2;
;         nc.cm[j] = (((kc >= wstart) && (kc < wstart + 16)) ? 0xFFFFu : 0u) | (((kc + 1 >= wstart) && (kc + 1 < wstart + 16)) ? 0xFFFF0000u : 0u);
;     }
;     nc.blane = (unsigned)(size_t)(LAS unsigned char*)smem + 49152u + (unsigned)((16 + (cs + gq * 4 - qcol + 15)) * 4);
;     ...
;     asm volatile("s_waitcnt lgkmcnt(0)" ::: "memory"); __builtin_amdgcn_s_barrier(); asm volatile("" ::: "memory");
;     ADMA(0);
;     if (ntile > 1) ADMA(1);
;     if (!ISA) {
;         for (int i = tid; i < 15 * 64; i += 256) { const int dr = i >> 6, dc = (i & 63) - 16; rpbl[i] = ((dc >= 0 && dc < 31) ? p.rpb[hh * 465 + dr * 31 + dc] * L2E : 0.f) - M2; }
	v_lshl_add_u64 v[24:25], v[104:105], 0, v[22:23]
	s_mov_b32 m0, s0
	v_readfirstlane_b32 s0, v26
	global_load_lds_dwordx4 v[24:25], off
	v_lshl_add_u64 v[24:25], v[106:107], 0, v[22:23]
	s_mov_b32 m0, s0
	v_add_u32_e32 v28, 0x6000, v21
	global_load_lds_dwordx4 v[24:25], off
	v_lshlrev_b64 v[24:25], 1, v[102:103]
	v_readfirstlane_b32 s0, v28
	v_add_u32_e32 v28, 0x6400, v21
	v_lshl_add_u64 v[26:27], v[108:109], 0, v[24:25]
	s_mov_b32 m0, s0
	v_readfirstlane_b32 s0, v28
	global_load_lds_dwordx4 v[26:27], off
	s_mov_b32 m0, s0
	s_mov_b64 s[0:1], 0x10000
	v_add_u32_e32 v32, 0x2000, v21
	v_lshl_add_u64 v[24:25], v[110:111], 0, v[24:25]
	v_lshl_add_u64 v[22:23], v[22:23], 0, s[0:1]
	v_readfirstlane_b32 s0, v32
	global_load_lds_dwordx4 v[24:25], off
	v_lshl_add_u64 v[28:29], v[104:105], 0, v[22:23]
	s_mov_b32 m0, s0
	v_lshl_add_u64 v[22:23], v[106:107], 0, v[22:23]
	global_load_lds_dwordx4 v[28:29], off
	v_add_u32_e32 v28, 0x2400, v21
	s_mov_b64 s[6:7], 0x80
	v_readfirstlane_b32 s0, v28
	s_mov_b32 m0, s0
	v_and_b32_e32 v103, 63, v30
	global_load_lds_dwordx4 v[22:23], off
	v_lshl_add_u64 v[22:23], v[26:27], 0, s[6:7]
	v_add_u32_e32 v26, 0x8000, v21
	v_add_u32_e32 v21, 0x8400, v21
	v_readfirstlane_b32 s0, v26
	s_mov_b32 m0, s0
	v_readfirstlane_b32 s0, v21
	global_load_lds_dwordx4 v[22:23], off
	v_lshl_add_u64 v[22:23], v[24:25], 0, s[6:7]
	s_mov_b32 m0, s0
	s_mul_i32 s6, s5, 0x1d1
	global_load_lds_dwordx4 v[22:23], off
	v_and_b32_e32 v23, 0xff, v30
	v_add_u32_e32 v22, -16, v103
	s_add_i32 s6, s6, -16
	v_mul_u32_u24_e32 v24, 31, v31
	v_lshlrev_b32_e32 v21, 3, v18
	v_cmp_gt_u32_e64 s[0:1], 31, v22
	v_lshl_add_u32 v22, v23, 2, v117
	v_add3_u32 v98, s6, v24, v103
	v_or_b32_e32 v23, 0xffffff00, v23
	v_mov_b32_e32 v26, 0
	v_mov_b32_e32 v27, 0
	v_mov_b32_e32 v28, 0
	v_mov_b32_e32 v29, 0
	v_and_b32_e32 v32, 0xff, v30
	s_movk_i32 s8, 0xc0
	v_lshl_add_u64 v[24:25], v[98:99], 2, s[80:81]
	v_cmp_gt_u32_e64 s[8:9], s8, v32
	s_and_saveexec_b64 s[6:7], s[0:1]
	global_load_dword v26, v[24:25], off
	global_load_dword v27, v[24:25], off offset:496
	global_load_dword v28, v[24:25], off offset:992
	s_and_b64 exec, exec, s[8:9]
	global_load_dword v29, v[24:25], off offset:1488
	s_mov_b64 exec, s[6:7]
	s_waitcnt vmcnt(0)
	v_mul_f32_e32 v26, 0x3fb8aa3b, v26
	v_mul_f32_e32 v27, 0x3fb8aa3b, v27
	v_mul_f32_e32 v28, 0x3fb8aa3b, v28
	v_mul_f32_e32 v29, 0x3fb8aa3b, v29
	v_sub_f32_e32 v26, v26, v113
	v_sub_f32_e32 v27, v27, v113
	v_sub_f32_e32 v28, v28, v113
	v_sub_f32_e32 v29, v29, v113
	ds_write_b32 v22, v26
	ds_write_b32 v22, v27 offset:1024
	ds_write_b32 v22, v28 offset:2048
	s_and_saveexec_b64 s[6:7], s[8:9]
	ds_write_b32 v22, v29 offset:3072
	s_or_b64 exec, exec, s[6:7]
	v_or_b32_e32 v22, v20, v112
	v_med3_u32 v20, v20, 8, 40
	v_add_u32_e32 v20, -8, v20
	v_med3_u32 v23, v22, 8, 56
	v_lshlrev_b32_e32 v98, 2, v18
	v_add_u32_e32 v24, v20, v98
	v_add_u32_e32 v25, 8, v23
	v_add_u32_e32 v23, -8, v23
	v_cmp_lt_u32_e64 s[0:1], v24, v25
	v_or_b32_e32 v26, 1, v24
	v_cmp_ge_u32_e64 s[20:21], v24, v23
	v_cmp_lt_u32_e64 s[6:7], v26, v25
	v_add_u32_e32 v29, 16, v24
	s_and_b64 s[0:1], s[20:21], s[0:1]
	v_cmp_ge_u32_e64 s[20:21], v26, v23
	v_or_b32_e32 v27, 2, v24
	v_or_b32_e32 v28, 3, v24
	v_add_u32_e32 v30, 17, v24
	v_or_b32_e32 v31, 2, v29
	v_add_u32_e32 v32, 19, v24
	s_and_b64 s[6:7], s[20:21], s[6:7]
	v_cmp_lt_u32_e64 s[8:9], v27, v25
	v_cmp_lt_u32_e64 s[10:11], v28, v25
	v_cmp_lt_u32_e64 s[12:13], v29, v25
	v_cmp_lt_u32_e64 s[14:15], v30, v25
	v_cmp_lt_u32_e64 s[16:17], v31, v25
	v_cmp_lt_u32_e64 s[18:19], v32, v25
	v_cndmask_b32_e64 v25, 0, v119, s[6:7]
	v_cmp_ge_u32_e64 s[6:7], v27, v23
	s_and_b64 s[6:7], s[6:7], s[8:9]
	v_cmp_ge_u32_e64 s[8:9], v28, v23
	s_and_b64 s[8:9], s[8:9], s[10:11]
	v_cmp_ge_u32_e64 s[10:11], v30, v23
	v_cndmask_b32_e64 v26, 0, v119, s[8:9]
	v_cmp_ge_u32_e64 s[8:9], v29, v23
	s_and_b64 s[10:11], s[10:11], s[14:15]
	v_cndmask_b32_e64 v28, 0, v120, s[0:1]
	s_and_b64 s[8:9], s[8:9], s[12:13]
	v_cndmask_b32_e64 v27, 0, v119, s[10:11]
	v_cmp_ge_u32_e64 s[10:11], v31, v23
	v_cmp_ge_u32_e64 s[12:13], v32, v23
	v_or_b32_e32 v125, v25, v28
	v_cndmask_b32_e64 v25, 0, v120, s[6:7]
	v_sub_u32_e32 v22, v24, v22
	s_and_b64 s[10:11], s[10:11], s[16:17]
	s_and_b64 s[12:13], s[12:13], s[18:19]
	v_or_b32_e32 v126, v26, v25
	v_cndmask_b32_e64 v25, 0, v120, s[8:9]
	v_min_i32_e32 v19, 0x78, v19
	v_cndmask_b32_e64 v23, 0, v119, s[12:13]
	v_or_b32_e32 v127, v27, v25
	v_cndmask_b32_e64 v25, 0, v120, s[10:11]
	v_lshl_add_u32 v129, v22, 2, v115
	v_lshrrev_b32_e32 v22, 1, v112
	v_cndmask_b32_e64 v137, v19, 0, vcc
	v_med3_i32 v19, v101, 3, v121
	v_or_b32_e32 v128, v25, v23
	v_xor_b32_e32 v25, v18, v22
	v_add_u32_e32 v138, -3, v19
	v_add_u32_e32 v140, 5, v19
	v_add_u16_e32 v19, v20, v112
	v_lshlrev_b32_e32 v131, 4, v25
	v_bitop3_b32 v25, v18, v22, 4 bitop3:0x36
	v_lshrrev_b16_e32 v19, 1, v19
	v_or_b32_e32 v23, 4, v18
	v_lshlrev_b32_e32 v132, 4, v25
	v_lshrrev_b32_e32 v25, 5, v103
	v_bitop3_b32 v18, v19, v18, 7 bitop3:0x6c
	v_xor_b32_e32 v26, v25, v22
	v_lshlrev_b32_e32 v142, 4, v18
	v_bitop3_b32 v18, v19, v23, 7 bitop3:0x6c
	v_lshlrev_b32_e32 v130, 7, v112
	v_and_b32_e32 v21, 8, v21
	v_lshlrev_b32_e32 v26, 4, v26
	v_lshlrev_b32_e32 v143, 4, v18
	v_lshrrev_b32_e32 v18, 3, v24
	v_or3_b32 v134, v26, v130, v21
	v_bitop3_b32 v26, v25, v22, 2 bitop3:0x36
	v_xor_b32_e32 v18, v18, v22
	v_lshlrev_b32_e32 v135, 4, v26
	v_bitop3_b32 v26, v25, v22, 4 bitop3:0x36
	v_lshlrev_b32_e32 v144, 4, v18
	v_lshlrev_b32_e32 v18, 1, v24
	v_lshlrev_b32_e32 v26, 4, v26
	v_and_or_b32 v145, v18, 8, v130
	v_lshrrev_b32_e32 v18, 3, v29
	v_or_b32_e32 v133, v21, v130
	v_bitop3_b32 v25, v25, v22, 6 bitop3:0x36
	v_add_lshl_u32 v141, v20, v112, 7
	v_xor_b32_e32 v18, v18, v22
	v_or3_b32 v147, v130, v26, v21
	v_mov_b32_e32 v20, v99
	v_mov_b32_e32 v21, v99
	v_lshlrev_b32_e32 v136, 4, v25
	v_lshlrev_b32_e32 v146, 4, v18
	v_mov_b32_e32 v18, v99
	v_mov_b32_e32 v19, v99
	v_mov_b32_e32 v50, 0
	v_mov_b64_e32 v[24:25], v[20:21]
	v_mov_b64_e32 v[28:29], v[20:21]
	v_mov_b64_e32 v[32:33], v[20:21]
	v_mov_b64_e32 v[36:37], v[20:21]
	v_mov_b64_e32 v[40:41], v[20:21]
	v_mov_b64_e32 v[44:45], v[20:21]
	v_mov_b64_e32 v[48:49], v[20:21]
	s_mov_b32 s26, 2
	v_add_u32_e32 v139, 8, v137
	s_movk_i32 s8, 0x1e40
	v_mov_b64_e32 v[22:23], v[18:19]
	v_mov_b64_e32 v[26:27], v[18:19]
	v_mov_b64_e32 v[30:31], v[18:19]
	v_mov_b64_e32 v[34:35], v[18:19]
	v_mov_b64_e32 v[38:39], v[18:19]
	v_mov_b64_e32 v[42:43], v[18:19]
	v_mov_b64_e32 v[46:47], v[18:19]
	v_mov_b32_e32 v51, v50
	v_mov_b32_e32 v52, v50
	v_mov_b32_e32 v53, v50
	v_mov_b32_e32 v54, v50
	v_mov_b32_e32 v55, v50
	v_mov_b32_e32 v56, v50
	v_mov_b32_e32 v57, v50
	s_cmpk_eq_i32 s8, 0x2140
	s_mov_b64 s[0:1], -1
	s_cbranch_scc1 .LBB0_386

; template <int NQ, int NKF, int MODE> ...
;     ...
;     f32x4 s[NQ][NKF];
;     const int krow = koff + l15, ksw = (krow >> 1) & 7;
;     const unsigned kad0 = kb_ + (unsigned)(krow * 128 + ((gq ^ ksw) << 4)), kad1 = kb_ + (unsigned)(krow * 128 + (((4 + gq) ^ ksw) << 4));
;     bf16x8 kfr[2][NKF];
; #pragma unroll
;     for (int ks = 0; ks < 2; ++ks)
; #pragma unroll
;         for (int kf = 0; kf < NKF; ++kf) AT_DSR128(kfr[ks][kf], (ks ? kad1 : kad0), kf * 2048);
;     float bv[NQ][NKF * 4];
;     if (MODE == 2) {
; #pragma unroll
;         for (int q = 0; q < NQ; ++q) {
;             int drq = qpos0 - q; drq = drq < 0 ? 0 : (drq > 14 ? 14 : drq);
;             const unsigned ba = nc.blane + (unsigned)(drq * 256);
; #pragma unroll
;             for (int kf = 0; kf < NKF; ++kf)
; #pragma unroll
;                 for (int r = 0; r < 4; ++r) AT_DSR32(bv[q][kf * 4 + r], ba, (kf * 16 + r) * 4);
;         }
;     }
;     const int vsw = (l15 >> 1) & 7;
;     i32x2 vlo[NKF / 2][4], vhi[NKF / 2][4];
; #pragma unroll
;     for (int q = 0; q < NQ; ++q)
; #pragma unroll
;         for (int kf = 0; kf < NKF; ++kf) s[q][kf] = (f32x4){0.f, 0.f, 0.f, 0.f};
;     if (MODE == 2) AT_LW((NQ * NKF * 4 > 15 ? 15 : NQ * NKF * 4)); else AT_LW(0);
; #pragma unroll
;     for (int ks = 0; ks < 2; ++ks)
; #pragma unroll
;         for (int kf = 0; kf < NKF; ++kf)
; #pragma unroll
;             for (int q = 0; q < NQ; ++q) s[q][kf] = mfma16(kfr[ks][kf], qf[q][ks], s[q][kf]);
;     __builtin_amdgcn_sched_barrier(0);
; #pragma unroll
;     for (int t = 0; t < NKF / 2; ++t) {
;         const int ko = koff + 32 * t + 4 * gq, ko2 = ko + 16;
;         const unsigned va = vb_ + (unsigned)(l15 * 128 + (((ko >> 3) ^ vsw) << 4) + ((ko & 4) << 1));
;         const unsigned vh = vb_ + (unsigned)(l15 * 128 + (((ko2 >> 3) ^ vsw) << 4) + ((ko2 & 4) << 1));
; #pragma unroll
;         for (int df = 0; df < 4; ++df) { AT_DSR64(vlo[t][df], va, df * 2048); AT_DSR64(vhi[t][df], vh, df * 2048); }
;     }
;     if (MODE == 2) AT_LW(NKF * 4);
;     bf16x8 pb[NQ][NKF / 2];
; #pragma unroll
;     for (int q = 0; q < NQ; ++q) {
;         unsigned ub = 0; unsigned qm = 0xFFFFFFFFu;
;         if (MODE == 1) ub = (unsigned)((qpos0 + q * 16) - (kpos0 + gq * 4) + 128);
;         if (MODE == 2) qm = ((kpos0 >> q) & 1) ? 0xFFFFFFFFu : 0u;
; #pragma unroll
;         for (int kf = 0; kf < NKF; ++kf)
; #pragma unroll
.LBB0_393:
	v_add_u32_e32 v74, v150, v130
	v_add_u32_e32 v70, v74, v131
	v_add_u32_e32 v86, v74, v132
	ds_read_b128 v[58:61], v70 offset:0
	ds_read_b128 v[62:65], v70 offset:0x800
	ds_read_b128 v[66:69], v70 offset:0x1000
	ds_read_b128 v[70:73], v70 offset:0x1800
	ds_read_b128 v[74:77], v86 offset:0
	ds_read_b128 v[78:81], v86 offset:0x800
	ds_read_b128 v[82:85], v86 offset:0x1000
	ds_read_b128 v[86:89], v86 offset:0x1800
	s_nop 0
	s_nop 0
	s_waitcnt lgkmcnt(7)
	v_mfma_f32_16x16x32_bf16 v[90:93], v[58:61], v[2:5], 0
	v_mfma_f32_16x16x32_bf16 v[58:61], v[58:61], v[10:13], 0
	s_waitcnt lgkmcnt(6)
	v_mfma_f32_16x16x32_bf16 v[94:97], v[62:65], v[2:5], 0
	v_mfma_f32_16x16x32_bf16 v[62:65], v[62:65], v[10:13], 0
	s_waitcnt lgkmcnt(5)
	v_mfma_f32_16x16x32_bf16 v[152:155], v[66:69], v[2:5], 0
	v_mfma_f32_16x16x32_bf16 v[66:69], v[66:69], v[10:13], 0
	s_waitcnt lgkmcnt(4)
	v_mfma_f32_16x16x32_bf16 v[156:159], v[70:73], v[2:5], 0
	v_mfma_f32_16x16x32_bf16 v[70:73], v[70:73], v[10:13], 0
	s_waitcnt lgkmcnt(3)
	v_mfma_f32_16x16x32_bf16 v[90:93], v[74:77], v[6:9], v[90:93]
	v_mfma_f32_16x16x32_bf16 v[58:61], v[74:77], v[14:17], v[58:61]
	s_waitcnt lgkmcnt(2)
	v_mfma_f32_16x16x32_bf16 v[74:77], v[78:81], v[6:9], v[94:97]
	v_mfma_f32_16x16x32_bf16 v[62:65], v[78:81], v[14:17], v[62:65]
	s_waitcnt lgkmcnt(1)
	v_mfma_f32_16x16x32_bf16 v[78:81], v[82:85], v[6:9], v[152:155]
	v_mfma_f32_16x16x32_bf16 v[66:69], v[82:85], v[14:17], v[66:69]
	s_waitcnt lgkmcnt(0)
	v_mfma_f32_16x16x32_bf16 v[82:85], v[86:89], v[6:9], v[156:159]
	v_mfma_f32_16x16x32_bf16 v[70:73], v[86:89], v[14:17], v[70:73]
	v_add_u32_e32 v151, v148, v133
	s_nop 0
	v_add_u32_e32 v156, v134, v148
	v_add_u32_e32 v158, v151, v135
	v_add_u32_e32 v172, v147, v148
	v_add_u32_e32 v151, v151, v136
	v_fma_f32 v74, v74, s63, -v113
	ds_read_b64 v[86:87], v156 offset:0
	ds_read_b64 v[88:89], v158 offset:0
	ds_read_b64 v[94:95], v156 offset:0x800
	ds_read_b64 v[96:97], v158 offset:0x800
	ds_read_b64 v[152:153], v156 offset:0x1000
	ds_read_b64 v[154:155], v158 offset:0x1000
	ds_read_b64 v[156:157], v156 offset:0x1800
	ds_read_b64 v[158:159], v158 offset:0x1800
	ds_read_b64 v[160:161], v172 offset:0
	ds_read_b64 v[162:163], v151 offset:0
	ds_read_b64 v[164:165], v172 offset:0x800
	ds_read_b64 v[166:167], v151 offset:0x800
	ds_read_b64 v[168:169], v172 offset:0x1000
	ds_read_b64 v[170:171], v151 offset:0x1000
	ds_read_b64 v[172:173], v172 offset:0x1800
	ds_read_b64 v[174:175], v151 offset:0x1800
	v_exp_f32_e32 v151, v74
	v_fma_f32 v74, v75, s63, -v113
	v_exp_f32_e32 v176, v74
	v_fma_f32 v74, v76, s63, -v113
	v_exp_f32_e32 v177, v74
	v_fma_f32 v74, v77, s63, -v113
	v_exp_f32_e32 v77, v74
	v_fma_f32 v74, v78, s63, -v113
	v_exp_f32_e32 v78, v74
	v_fma_f32 v74, v79, s63, -v113
	v_exp_f32_e32 v79, v74
	v_fma_f32 v74, v80, s63, -v113
	v_exp_f32_e32 v80, v74
	v_fma_f32 v74, v81, s63, -v113
	v_exp_f32_e32 v81, v74
	v_fma_f32 v74, v82, s63, -v113
	v_exp_f32_e32 v82, v74
	v_fma_f32 v74, v83, s63, -v113
	v_fma_f32 v90, v90, s63, -v113
	v_fma_f32 v91, v91, s63, -v113
	v_fma_f32 v92, v92, s63, -v113
	v_fma_f32 v93, v93, s63, -v113
	v_exp_f32_e32 v83, v74
	v_fma_f32 v74, v84, s63, -v113
	v_fma_f32 v58, v58, s63, -v113
	v_fma_f32 v59, v59, s63, -v113
	v_fma_f32 v60, v60, s63, -v113
	v_fma_f32 v61, v61, s63, -v113
	v_fma_f32 v62, v62, s63, -v113
	v_fma_f32 v63, v63, s63, -v113
	v_fma_f32 v64, v64, s63, -v113
	v_fma_f32 v65, v65, s63, -v113
	v_exp_f32_e32 v90, v90
	v_exp_f32_e32 v91, v91
	v_exp_f32_e32 v92, v92
	v_exp_f32_e32 v93, v93
	v_exp_f32_e32 v84, v74
	v_fma_f32 v74, v85, s63, -v113
	v_exp_f32_e32 v58, v58
	v_exp_f32_e32 v59, v59
	v_exp_f32_e32 v60, v60
	v_exp_f32_e32 v61, v61
	v_exp_f32_e32 v62, v62
	v_exp_f32_e32 v63, v63
	v_exp_f32_e32 v64, v64
	v_exp_f32_e32 v65, v65
	v_fma_f32 v66, v66, s63, -v113
	v_fma_f32 v67, v67, s63, -v113
	v_fma_f32 v68, v68, s63, -v113
	v_fma_f32 v69, v69, s63, -v113
	v_fma_f32 v70, v70, s63, -v113
	v_fma_f32 v71, v71, s63, -v113
	v_fma_f32 v72, v72, s63, -v113
	v_fma_f32 v73, v73, s63, -v113
	v_exp_f32_e32 v85, v74
	v_exp_f32_e32 v66, v66
	v_exp_f32_e32 v67, v67
	v_exp_f32_e32 v68, v68
	v_exp_f32_e32 v69, v69
	v_exp_f32_e32 v70, v70
	v_exp_f32_e32 v71, v71
	v_exp_f32_e32 v72, v72
	v_exp_f32_e32 v73, v73
	s_waitcnt lgkmcnt(0)
	v_cvt_pk_bf16_f32 v74, v90, v91
	v_cvt_pk_bf16_f32 v75, v92, v93
	v_cvt_pk_bf16_f32 v76, v151, v176
	v_cvt_pk_bf16_f32 v77, v177, v77
	v_cvt_pk_bf16_f32 v58, v58, v59
	v_cvt_pk_bf16_f32 v59, v60, v61
	v_cvt_pk_bf16_f32 v60, v62, v63
	v_cvt_pk_bf16_f32 v61, v64, v65
	v_cvt_pk_bf16_f32 v176, v78, v79
	v_cvt_pk_bf16_f32 v177, v80, v81
	v_cvt_pk_bf16_f32 v178, v82, v83
	v_cvt_pk_bf16_f32 v179, v84, v85
	v_cvt_pk_bf16_f32 v180, v66, v67
	v_cvt_pk_bf16_f32 v181, v68, v69
	v_cvt_pk_bf16_f32 v182, v70, v71
	v_cvt_pk_bf16_f32 v183, v72, v73
	s_mov_b32 s38, s36
	s_mov_b32 s39, s36
	s_mov_b32 s37, s36
	v_mov_b64_e32 v[64:65], s[38:39]
	v_mov_b64_e32 v[62:63], s[36:37]
	v_mfma_f32_16x16x32_bf16 v[82:85], v[86:89], v[74:77], v[46:49]
	s_nop 0
	v_mfma_f32_16x16x32_bf16 v[66:69], v[62:65], v[74:77], v[50:53]
	v_mfma_f32_16x16x32_bf16 v[70:73], v[62:65], v[58:61], v[54:57]
	v_mfma_f32_16x16x32_bf16 v[86:89], v[86:89], v[58:61], v[42:45]
	v_mfma_f32_16x16x32_bf16 v[90:93], v[94:97], v[74:77], v[38:41]
	v_mfma_f32_16x16x32_bf16 v[94:97], v[94:97], v[58:61], v[34:37]
	v_mfma_f32_16x16x32_bf16 v[184:187], v[152:155], v[74:77], v[30:33]
	v_mfma_f32_16x16x32_bf16 v[152:155], v[152:155], v[58:61], v[26:29]
	v_mfma_f32_16x16x32_bf16 v[74:77], v[156:159], v[74:77], v[22:25]
	v_mfma_f32_16x16x32_bf16 v[156:159], v[156:159], v[58:61], v[18:21]
	v_mfma_f32_16x16x32_bf16 v[78:81], v[62:65], v[176:179], v[66:69]
	v_mfma_f32_16x16x32_bf16 v[58:61], v[62:65], v[180:183], v[70:73]
	v_mfma_f32_16x16x32_bf16 v[82:85], v[160:163], v[176:179], v[82:85]
	v_mfma_f32_16x16x32_bf16 v[62:65], v[160:163], v[180:183], v[86:89]
	v_mfma_f32_16x16x32_bf16 v[86:89], v[164:167], v[176:179], v[90:93]
	v_mfma_f32_16x16x32_bf16 v[66:69], v[164:167], v[180:183], v[94:97]
	v_mfma_f32_16x16x32_bf16 v[90:93], v[168:171], v[176:179], v[184:187]
	v_mfma_f32_16x16x32_bf16 v[70:73], v[168:171], v[180:183], v[152:155]
	v_mfma_f32_16x16x32_bf16 v[94:97], v[172:175], v[176:179], v[74:77]
	v_mfma_f32_16x16x32_bf16 v[74:77], v[172:175], v[180:183], v[156:159]
	s_cbranch_execnz .LBB0_392

; template <bool ISA>
; __device__ __forceinline__ void attn_unit(const Params& p, unsigned char* smem, int b, int hh, int blk) {
;     constexpr int NQ = 2;
;     constexpr int QSTR = ISA ? 16 : 64;
;     const int tid = otid() & 255, lane = tid & 63, wid = tid >> 6, l15 = lane & 15, gq = lane >> 4;
;     int nl, tbase;
;     if (ISA) {
;         const int start = blk * 128;
;         const int j0 = start >= 128 ? 0 : 2, j1 = (start + 256 <= SEQ) ? 6 : 4;
;         nl = j1 - j0; tbase = start - 128 + 64 * j0;
;     } else {
;         int rs = 2 * blk - 4; rs = rs < 0 ? 0 : (rs > 119 ? 119 : rs);
;         nl = 9; tbase = rs * 64;
;     }
;     const int ntile = nl + 4;
;     const bf16_t* kbase; const bf16_t* vbase; int ldk;
;     if (ISA) { const int g = hh >> 2; kbase = p.ka + (size_t)(b * TT) * 128 + g * 64; ldk = 128; vbase = p.vta + (size_t)((b * 2 + g) * 64) * TT; }
;     else { kbase = p.kb + (size_t)(b * TT) * 512 + hh * 64; ldk = 512; vbase = p.vtb + (size_t)((b * 8 + hh) * 64) * TT; }
;     float* rpbl = (float*)(smem + 49152);
;     const float M2 = p.attm[ISA ? hh : 8 + hh], negM2 = -M2;
;     const int qt0 = ISA ? blk * 128 + wid * 32 : blk * 128 + wid * 16;
;     bf16x8 qf[NQ][2];
;     {
;         const bf16_t* qsrc = ISA ? p.qa : p.qb;
; #pragma unroll
;         for (int q = 0; q < NQ; ++q)
; #pragma unroll
;             for (int ks = 0; ks < 2; ++ks)
;                 qf[q][ks] = *(const bf16x8*)(qsrc + (size_t)(b * TT + qt0 + q * QSTR + l15) * 512 + hh * 64 + ks * 32 + gq * 8);
;     }
;     f32x4 osum[NQ]; f32x4 o[NQ][4];
; #pragma unroll
;     for (int q = 0; q < NQ; ++q) {
;         const float l0 = ISA ? __builtin_amdgcn_exp2f(p.sink[hh] * L2E - M2) : 0.f;
;         osum[q] = (f32x4){l0, l0, l0, l0};
; #pragma unroll
;         for (int df = 0; df < 4; ++df) o[q][df] = (f32x4){0.f, 0.f, 0.f, 0.f};
;     }
;     const int qcol = wid * 16 + l15;
;     int cs = wid * 16 - 8; cs = cs < 0 ? 0 : (cs > 32 ? 32 : cs);
;     int wstart = qcol - 8; wstart = wstart < 0 ? 0 : (wstart > 48 ? 48 : wstart);
;     NaConst nc;
; #pragma unroll
;     for (int j = 0; j < 4; ++j) {
;         const int kc = cs + (j >> 1) * 16 + gq * 4 + (j & 1) * 2;
;         nc.cm[j] = (((kc >= wstart) && (kc < wstart + 16)) ? 0xFFFFu : 0u) | (((kc + 1 >= wstart) && (kc + 1 < wstart + 16)) ? 0xFFFF0000u : 0u);
;     }
.LBB0_401:
	s_and_b64 vcc, exec, s[0:1]
	s_cbranch_vccz .LBB0_425
	v_lshl_add_u32 v2, s4, 1, v1
	v_mov_b32_e32 v31, v0
	v_ashrrev_i32_e32 v30, 2, v2
	s_lshr_b32 s5, s5, 1
	v_bfe_u32 v19, v31, 6, 2
	s_lshl_b32 s0, s22, 2
	v_lshlrev_b32_e32 v18, 7, v30
	v_lshlrev_b32_e32 v33, 5, v19
	s_and_b32 s6, s0, 4
	s_mul_i32 s0, s5, 0x2100
	v_or_b32_e32 v84, v33, v18
	v_and_or_b32 v82, v2, 3, s6
	v_and_b32_e32 v83, 15, v31
	v_add_u32_e32 v2, s0, v84
	v_readlane_b32 s8, v248, 11
	s_lshl_b32 s1, s6, 4
	s_lshl_b32 s7, s5, 7
	v_or_b32_e32 v2, v2, v83
	v_lshlrev_b32_e32 v4, 7, v82
	v_mov_b32_e32 v5, v99
	v_readlane_b32 s9, v248, 12
	s_or_b32 s1, s1, s7
	v_and_b32_e32 v6, 48, v31
	v_lshl_add_u64 v[4:5], s[8:9], 0, v[4:5]
	v_mov_b32_e32 v7, v99
	v_ashrrev_i32_e32 v3, 31, v2
	s_mul_i32 s0, s5, 0x210000
	v_readlane_b32 s8, v248, 5
	v_lshl_add_u64 v[4:5], v[4:5], 0, v[6:7]
	v_lshlrev_b64 v[6:7], 10, v[2:3]
	v_or_b32_e32 v2, 16, v2
	v_readlane_b32 s9, v248, 6
	s_add_u32 s7, s8, s0
	v_ashrrev_i32_e32 v3, 31, v2
	s_addc_u32 s8, s9, 0
	s_mulk_i32 s1, 0x4200
	v_readlane_b32 s0, v248, 24
	v_lshlrev_b64 v[2:3], 10, v[2:3]
	s_add_u32 s0, s0, s1
	v_readlane_b32 s1, v248, 0
	v_readlane_b32 s10, v248, 20
	v_lshlrev_b32_e32 v21, 2, v82
	v_lshl_add_u64 v[14:15], v[4:5], 0, v[6:7]
	v_lshl_add_u64 v[10:11], v[4:5], 0, v[2:3]
	s_addc_u32 s1, s1, 0
	v_readlane_b32 s11, v248, 21
	s_lshl_b32 s6, s6, 5
	global_load_dwordx4 v[2:5], v[14:15], off offset:64
	global_load_dwordx4 v[6:9], v[10:11], off
	s_nop 0
	global_load_dwordx4 v[10:13], v[10:11], off offset:64
	s_nop 0
	global_load_dword v100, v21, s[10:11]
	s_nop 0
	global_load_dwordx4 v[14:17], v[14:15], off
	s_nop 0
	global_load_dword v34, v21, s[78:79]
	s_add_u32 s6, s7, s6
	v_bfe_u32 v21, v31, 3, 3
	s_addc_u32 s7, s8, 0
	v_readfirstlane_b32 s8, v19
	v_lshl_or_b32 v19, v19, 4, v21
	v_or_b32_e32 v21, 8, v19
	v_bfe_u32 v32, v31, 4, 2
	v_lshrrev_b32_e32 v22, 1, v21
	v_bitop3_b32 v24, v32, v31, 7 bitop3:0x78
	v_xor_b32_e32 v26, v22, v31
	v_lshlrev_b32_e32 v22, 8, v19
	s_waitcnt lgkmcnt(0)
	v_mov_b32_e32 v23, v99
	v_lshl_add_u64 v[22:23], s[6:7], 0, v[22:23]
	v_lshlrev_b32_e32 v24, 4, v24
	v_mov_b32_e32 v25, v99
	v_lshl_add_u64 v[90:91], v[22:23], 0, v[24:25]
	v_lshlrev_b32_e32 v22, 8, v21
	v_mov_b32_e32 v23, v99
	v_lshlrev_b32_e32 v26, 4, v26
	v_cmp_lt_i32_e32 vcc, 0, v30
	v_lshl_add_u64 v[22:23], s[6:7], 0, v[22:23]
	v_and_b32_e32 v26, 0x70, v26
	v_mov_b32_e32 v27, v99
	v_cndmask_b32_e64 v85, 2, 0, vcc
	v_lshl_add_u64 v[92:93], v[22:23], 0, v[26:27]
	v_mov_b64_e32 v[22:23], s[0:1]
	s_movk_i32 s6, 0x4200
	v_add_u32_e32 v89, 0xffffff80, v18
	v_lshlrev_b32_e32 v20, 6, v85
	v_mad_u64_u32 v[28:29], s[0:1], v19, s6, v[22:23]
	v_mad_u64_u32 v[22:23], s[0:1], v21, s6, v[22:23]
	s_lshl_b32 s76, s8, 11
	v_add_u32_e32 v86, v20, v89
	v_lshl_add_u64 v[96:97], v[22:23], 0, v[26:27]
	v_add_u32_e32 v26, s76, v114
	v_ashrrev_i32_e32 v87, 31, v86
	v_readfirstlane_b32 s0, v26
	v_add_u32_e32 v19, 0x400, v26
	v_lshlrev_b64 v[22:23], 8, v[86:87]
	s_mov_b32 m0, s0
	v_readfirstlane_b32 s0, v19
	v_mov_b32_e32 v21, v99
	v_ashrrev_i32_e32 v19, 31, v18
	v_lshl_add_u64 v[94:95], v[28:29], 0, v[24:25]
	s_waitcnt lgkmcnt(0)
	s_barrier
; #define LAS __attribute__((address_space(3)))
; template <bool ISA>
; __device__ __forceinline__ void attn_unit(const Params& p, unsigned char* smem, int b, int hh, int blk) {
;     ...
;     f32x4 osum[NQ]; f32x4 o[NQ][4];
; #pragma unroll
;     for (int q = 0; q < NQ; ++q) {
;         const float l0 = ISA ? __builtin_amdgcn_exp2f(p.sink[hh] * L2E - M2) : 0.f;
;         osum[q] = (f32x4){l0, l0, l0, l0};
; #pragma unroll
;         for (int df = 0; df < 4; ++df) o[q][df] = (f32x4){0.f, 0.f, 0.f, 0.f};
;     }
;     const int qcol = wid * 16 + l15;
;     int cs = wid * 16 - 8; cs = cs < 0 ? 0 : (cs > 32 ? 32 : cs);
;     int wstart = qcol - 8; wstart = wstart < 0 ? 0 : (wstart > 48 ? 48 : wstart);
;     NaConst nc;
; #pragma unroll
;     for (int j = 0; j < 4; ++j) {
;         const int kc = cs + (j >> 1) * 16 + gq * 4 + (j & 1) * 2;
;         nc.cm[j] = (((kc >= wstart) && (kc < wstart + 16)) ? 0xFFFFu : 0u) | (((kc + 1 >= wstart) && (kc + 1 < wstart + 16)) ? 0xFFFF0000u : 0u);
;     }
;     nc.blane = (unsigned)(size_t)(LAS unsigned char*)smem + 49152u + (unsigned)((16 + (cs + gq * 4 - qcol + 15)) * 4);
;     ...
;     asm volatile("s_waitcnt lgkmcnt(0)" ::: "memory"); __builtin_amdgcn_s_barrier(); asm volatile("" ::: "memory");
;     ADMA(0);
;     if (ntile > 1) ADMA(1);
	v_lshl_add_u64 v[24:25], v[90:91], 0, v[22:23]
	v_lshl_add_u64 v[18:19], v[20:21], 0, v[18:19]
	global_load_lds_dwordx4 v[24:25], off
	v_lshl_add_u64 v[22:23], v[92:93], 0, v[22:23]
	s_mov_b32 m0, s0
	v_lshlrev_b64 v[18:19], 1, v[18:19]
	s_movk_i32 s6, 0xff00
	v_add_u32_e32 v21, 0x6000, v26
	global_load_lds_dwordx4 v[22:23], off
	v_lshl_add_u64 v[22:23], v[94:95], 0, v[18:19]
	s_mov_b32 s7, -1
	v_readfirstlane_b32 s0, v21
	v_lshl_add_u64 v[22:23], v[22:23], 0, s[6:7]
	s_mov_b32 m0, s0
	v_add_u32_e32 v21, 0x6400, v26
	global_load_lds_dwordx4 v[22:23], off
	v_lshl_add_u64 v[22:23], v[96:97], 0, v[18:19]
	v_readfirstlane_b32 s0, v21
	v_lshl_add_u64 v[22:23], v[22:23], 0, s[6:7]
	s_mov_b32 m0, s0
	v_add_u32_e32 v21, 0x2000, v26
	global_load_lds_dwordx4 v[22:23], off
	v_or_b32_e32 v22, 64, v86
	v_ashrrev_i32_e32 v23, 31, v22
	v_lshlrev_b64 v[22:23], 8, v[22:23]
	v_readfirstlane_b32 s0, v21
	v_add_u32_e32 v21, 0x2400, v26
	v_lshl_add_u64 v[24:25], v[90:91], 0, v[22:23]
	s_mov_b32 m0, s0
	v_readfirstlane_b32 s0, v21
	global_load_lds_dwordx4 v[24:25], off
	v_lshl_add_u64 v[22:23], v[92:93], 0, v[22:23]
	s_mov_b32 m0, s0
	v_or_b32_e32 v18, 0x80, v18
	v_add_u32_e32 v21, 0x8000, v26
	global_load_lds_dwordx4 v[22:23], off
	v_lshl_add_u64 v[22:23], v[94:95], 0, v[18:19]
	v_readfirstlane_b32 s0, v21
	v_add_u32_e32 v21, 0x8400, v26
	v_lshl_add_u64 v[22:23], v[22:23], 0, s[6:7]
	s_mov_b32 m0, s0
	v_lshl_add_u64 v[18:19], v[96:97], 0, v[18:19]
	v_readfirstlane_b32 s0, v21
	global_load_lds_dwordx4 v[22:23], off
	v_lshl_add_u64 v[18:19], v[18:19], 0, s[6:7]
	s_mov_b32 m0, s0
	v_cmp_gt_i32_e32 vcc, 63, v30
	global_load_lds_dwordx4 v[18:19], off
	s_nop 0
	v_cndmask_b32_e64 v18, 4, 6, vcc
	s_mov_b32 s0, 0x3fb8aa3b
	v_sub_u32_e32 v101, v18, v85
	s_waitcnt vmcnt(8)
	v_fma_f32 v18, v34, s0, -v100
	v_exp_f32_e32 v38, v18
	v_bfe_u32 v18, v31, 1, 3
	v_xor_b32_e32 v21, v32, v18
	v_lshlrev_b32_e32 v103, 4, v21
	v_bitop3_b32 v21, v32, v18, 4 bitop3:0x36
	v_lshlrev_b32_e32 v104, 4, v21
	v_bfe_u32 v21, v31, 5, 1
	s_movk_i32 s0, 0x110
	v_lshrrev_b32_e32 v19, 1, v31
	v_lshlrev_b32_e32 v88, 2, v32
	v_xor_b32_e32 v22, v21, v18
	v_bitop3_b32 v23, v21, v18, 2 bitop3:0x36
	v_bitop3_b32 v24, v21, v18, 4 bitop3:0x36
	v_bitop3_b32 v18, v21, v18, 6 bitop3:0x36
	v_or3_b32 v21, v33, v83, s0
	v_and_b32_e32 v19, 8, v19
	v_lshlrev_b32_e32 v22, 4, v22
	v_lshlrev_b32_e32 v23, 4, v23
	v_lshlrev_b32_e32 v24, 4, v24
	v_lshlrev_b32_e32 v18, 4, v18
	v_sub_u32_e32 v21, v21, v88
	s_movk_i32 s0, 0x6000
	v_mov_b32_e32 v62, v99
	v_mov_b32_e32 v63, v99
	v_mov_b32_e32 v64, v99
	v_mov_b32_e32 v65, v99
	v_and_b32_e32 v87, 63, v31
	v_sub_u32_e32 v110, v21, v20
	v_or3_b32 v111, v24, v19, s0
	v_or3_b32 v113, v22, v19, s0
	v_or3_b32 v125, v18, v19, s0
	v_or3_b32 v126, v23, v19, s0
	v_mov_b64_e32 v[58:59], v[62:63]
	v_mov_b64_e32 v[68:69], v[64:65]
	v_mov_b64_e32 v[30:31], v[62:63]
	v_mov_b64_e32 v[34:35], v[62:63]
	v_mov_b64_e32 v[18:19], v[62:63]
	v_mov_b64_e32 v[42:43], v[62:63]
	v_mov_b64_e32 v[22:23], v[62:63]
	v_mov_b64_e32 v[46:47], v[62:63]
	v_mov_b64_e32 v[50:51], v[62:63]
	v_mov_b64_e32 v[54:55], v[62:63]
	s_mov_b32 s72, 2
	s_mov_b32 s73, 0
	v_lshlrev_b32_e32 v98, 6, v82
	v_add_u32_e32 v102, 4, v101
	v_add_u32_e32 v105, 0xffffff9f, v84
	v_add_u32_e32 v106, 0x41, v84
	v_add_u32_e32 v107, 0x9f, v84
	v_add_u32_e32 v108, 0xffffff80, v84
	v_sub_u32_e32 v109, 0, v101
	v_lshl_add_u32 v112, v83, 7, v114
	s_mov_b64 s[82:83], 0
	v_mov_b64_e32 v[60:61], v[64:65]
	v_mov_b64_e32 v[66:67], v[62:63]
	v_mov_b64_e32 v[32:33], v[64:65]
	v_mov_b64_e32 v[36:37], v[64:65]
	v_mov_b64_e32 v[20:21], v[64:65]
	v_mov_b64_e32 v[44:45], v[64:65]
	v_mov_b64_e32 v[24:25], v[64:65]
	v_mov_b64_e32 v[48:49], v[64:65]
	v_mov_b64_e32 v[52:53], v[64:65]
	s_mov_b32 s8, 0
	v_mov_b64_e32 v[56:57], v[64:65]
	v_mov_b32_e32 v39, v38
	v_mov_b32_e32 v40, v38
	v_mov_b32_e32 v41, v38
	v_mov_b32_e32 v26, v38
	v_mov_b32_e32 v27, v38
	v_mov_b32_e32 v28, v38
	v_mov_b32_e32 v29, v38
	s_branch .LBB0_405

; template <int NQ, int NKF, int MODE> ...
;     ...
;     f32x4 s[NQ][NKF];
;     const int krow = koff + l15, ksw = (krow >> 1) & 7;
;     const unsigned kad0 = kb_ + (unsigned)(krow * 128 + ((gq ^ ksw) << 4)), kad1 = kb_ + (unsigned)(krow * 128 + (((4 + gq) ^ ksw) << 4));
;     bf16x8 kfr[2][NKF];
; #pragma unroll
;     for (int ks = 0; ks < 2; ++ks)
; #pragma unroll
;         for (int kf = 0; kf < NKF; ++kf) AT_DSR128(kfr[ks][kf], (ks ? kad1 : kad0), kf * 2048);
;     float bv[NQ][NKF * 4];
;     if (MODE == 2) {
; #pragma unroll
;         for (int q = 0; q < NQ; ++q) {
;             int drq = qpos0 - q; drq = drq < 0 ? 0 : (drq > 14 ? 14 : drq);
; template <bool ISA>
; __device__ __forceinline__ void attn_unit(const Params& p, unsigned char* smem, int b, int hh, int blk) {
;     ...
;     for (int ti = 0; ti < ntile; ++ti) {
;         if (ti + 1 < ntile) asm volatile("s_waitcnt vmcnt(4)" ::: "memory"); else asm volatile("s_waitcnt vmcnt(0)" ::: "memory");
;         asm volatile("s_waitcnt lgkmcnt(0)" ::: "memory"); __builtin_amdgcn_s_barrier(); asm volatile("" ::: "memory");
;         if (ti + 2 < ntile) ADMA(ti + 2);
;         const unsigned kb_ = ldsa + (unsigned)((ti % 3) * 8192), vb_ = ldsa + 24576u + (unsigned)((ti % 3) * 8192);
;         if (ti < nl) {
;             const int t0 = tbase + 64 * ti;
;             if (ISA) {
;                 const bool skip = (t0 > qt0 + 31 + 128) || (t0 + 63 < qt0 - 128);
;                 const bool inner = (t0 >= qt0 + 31 - 128) && (t0 + 63 <= qt0 + 128);
;                 if (inner) attn_tile<NQ, 4, 0>(kb_, vb_, 0, qf, osum, o, l15, gq, 0, 0, negM2, nc);
;                 else if (!skip) attn_tile<NQ, 4, 1>(kb_, vb_, 0, qf, osum, o, l15, gq, qt0 + l15, t0, negM2, nc);
;             } else {
;                 const int kr_ = t0 >> 6;
;                 const int r0q = 2 * blk, dr0 = kr_ - r0q + 7;
;                 int rs0 = r0q - 4; rs0 = rs0 < 0 ? 0 : (rs0 > 120 ? 120 : rs0);
;                 int rs1 = r0q + 1 - 4; rs1 = rs1 < 0 ? 0 : (rs1 > 120 ? 120 : rs1);
;                 const int qact = ((kr_ >= rs0 && kr_ < rs0 + 8) ? 1 : 0) | ((kr_ >= rs1 && kr_ < rs1 + 8) ? 2 : 0);
;                 attn_tile<NQ, 2, 2>(kb_, vb_, cs, qf, osum, o, l15, gq, dr0, qact, negM2, nc);
;             }
;         } else {
;             attn_tile<NQ, 4, 0>(kb_, vb_, 0, qf, osum, o, l15, gq, 0, 0, negM2, nc);
;         }
.LBB0_411:
	s_or_b64 exec, exec, s[6:7]
	s_mul_hi_u32 s0, s8, 0xaaaaaaab
	s_lshr_b32 s0, s0, 1
	s_mulk_i32 s0, 0x6000
	v_subrev_u32_e32 v127, s0, v111
	v_subrev_u32_e32 v129, s0, v113
	v_subrev_u32_e32 v128, s0, v125
	v_subrev_u32_e32 v130, s0, v126
	v_subrev_u32_e32 v131, s0, v104
	v_subrev_u32_e32 v132, s0, v103
	v_cmp_ge_u32_e64 s[0:1], s8, v101
	s_and_saveexec_b64 s[6:7], s[0:1]
	s_xor_b64 s[0:1], exec, s[6:7]
	s_cbranch_execz .LBB0_413
	v_add_u32_e32 v156, s73, v112
	v_add_u32_e32 v70, v156, v132
	ds_read_b128 v[58:61], v70 offset:0
	ds_read_b128 v[62:65], v70 offset:0x800
	ds_read_b128 v[66:69], v70 offset:0x1000
	ds_read_b128 v[70:73], v70 offset:0x1800
	v_add_u32_e32 v131, v156, v131
	ds_read_b128 v[74:77], v131 offset:0
	ds_read_b128 v[78:81], v131 offset:0x800
	ds_read_b128 v[132:135], v131 offset:0x1000
	ds_read_b128 v[136:139], v131 offset:0x1800
	s_nop 0
	s_waitcnt lgkmcnt(7)
	v_mfma_f32_16x16x32_bf16 v[140:143], v[58:61], v[14:17], 0
	v_mfma_f32_16x16x32_bf16 v[58:61], v[58:61], v[6:9], 0
	s_waitcnt lgkmcnt(6)
	v_mfma_f32_16x16x32_bf16 v[144:147], v[62:65], v[14:17], 0
	v_mfma_f32_16x16x32_bf16 v[62:65], v[62:65], v[6:9], 0
	s_waitcnt lgkmcnt(5)
	v_mfma_f32_16x16x32_bf16 v[148:151], v[66:69], v[14:17], 0
	v_mfma_f32_16x16x32_bf16 v[66:69], v[66:69], v[6:9], 0
	s_waitcnt lgkmcnt(4)
	v_mfma_f32_16x16x32_bf16 v[152:155], v[70:73], v[14:17], 0
	v_mfma_f32_16x16x32_bf16 v[70:73], v[70:73], v[6:9], 0
	s_waitcnt lgkmcnt(3)
	v_mfma_f32_16x16x32_bf16 v[140:143], v[74:77], v[2:5], v[140:143]
	v_mfma_f32_16x16x32_bf16 v[58:61], v[74:77], v[10:13], v[58:61]
	s_waitcnt lgkmcnt(2)
	v_mfma_f32_16x16x32_bf16 v[74:77], v[78:81], v[2:5], v[144:147]
	v_mfma_f32_16x16x32_bf16 v[62:65], v[78:81], v[10:13], v[62:65]
	s_waitcnt lgkmcnt(1)
	v_mfma_f32_16x16x32_bf16 v[78:81], v[132:135], v[2:5], v[148:151]
	v_mfma_f32_16x16x32_bf16 v[66:69], v[132:135], v[10:13], v[66:69]
	s_waitcnt lgkmcnt(0)
	v_mfma_f32_16x16x32_bf16 v[132:135], v[136:139], v[2:5], v[152:155]
	v_mfma_f32_16x16x32_bf16 v[70:73], v[136:139], v[10:13], v[70:73]
	v_add_u32_e32 v129, v156, v129
	v_add_u32_e32 v130, v156, v130
	v_add_u32_e32 v127, v156, v127
	v_fma_f32 v74, v74, s63, -v100
	ds_read_b64 v[136:137], v129 offset:0
	ds_read_b64 v[138:139], v130 offset:0
	ds_read_b64 v[144:145], v129 offset:0x800
	ds_read_b64 v[146:147], v130 offset:0x800
	ds_read_b64 v[148:149], v129 offset:0x1000
	ds_read_b64 v[150:151], v130 offset:0x1000
	ds_read_b64 v[152:153], v129 offset:0x1800
	ds_read_b64 v[154:155], v130 offset:0x1800
	v_add_u32_e32 v166, v156, v128
	ds_read_b64 v[128:129], v127 offset:0
	ds_read_b64 v[130:131], v166 offset:0
	ds_read_b64 v[156:157], v127 offset:0x800
	ds_read_b64 v[158:159], v166 offset:0x800
	ds_read_b64 v[160:161], v127 offset:0x1000
	ds_read_b64 v[162:163], v166 offset:0x1000
	ds_read_b64 v[164:165], v127 offset:0x1800
	v_fma_f32 v127, v140, s63, -v100
	v_fma_f32 v140, v141, s63, -v100
	v_fma_f32 v141, v142, s63, -v100
	v_fma_f32 v142, v143, s63, -v100
	v_exp_f32_e32 v143, v74
	v_fma_f32 v74, v75, s63, -v100
	v_exp_f32_e32 v168, v74
	v_fma_f32 v74, v76, s63, -v100
	v_exp_f32_e32 v169, v74
	v_fma_f32 v74, v77, s63, -v100
	v_exp_f32_e32 v77, v74
	v_fma_f32 v74, v78, s63, -v100
	v_exp_f32_e32 v78, v74
	v_fma_f32 v74, v79, s63, -v100
	v_exp_f32_e32 v79, v74
	v_fma_f32 v74, v80, s63, -v100
	v_exp_f32_e32 v80, v74
	v_fma_f32 v74, v81, s63, -v100
	v_exp_f32_e32 v81, v74
	v_fma_f32 v74, v132, s63, -v100
	v_exp_f32_e32 v127, v127
	v_exp_f32_e32 v140, v140
	v_exp_f32_e32 v132, v74
	v_fma_f32 v74, v133, s63, -v100
	v_exp_f32_e32 v133, v74
	v_fma_f32 v74, v134, s63, -v100
	v_exp_f32_e32 v134, v74
	v_fma_f32 v74, v135, s63, -v100
	v_fma_f32 v70, v70, s63, -v100
	v_exp_f32_e32 v135, v74
	v_cvt_pk_bf16_f32 v74, v127, v140
	v_exp_f32_e32 v127, v70
	v_fma_f32 v70, v71, s63, -v100
	v_cvt_pk_bf16_f32 v78, v78, v79
	v_cvt_pk_bf16_f32 v79, v80, v81
	v_cvt_pk_bf16_f32 v80, v132, v133
	v_fma_f32 v58, v58, s63, -v100
	v_fma_f32 v59, v59, s63, -v100
	v_fma_f32 v60, v60, s63, -v100
	v_fma_f32 v61, v61, s63, -v100
	v_fma_f32 v62, v62, s63, -v100
	v_fma_f32 v63, v63, s63, -v100
	v_fma_f32 v64, v64, s63, -v100
	v_fma_f32 v65, v65, s63, -v100
	v_exp_f32_e32 v132, v70
	v_fma_f32 v70, v72, s63, -v100
	v_exp_f32_e32 v58, v58
	v_exp_f32_e32 v59, v59
	v_exp_f32_e32 v60, v60
	v_exp_f32_e32 v61, v61
	v_exp_f32_e32 v62, v62
	v_exp_f32_e32 v63, v63
	v_exp_f32_e32 v64, v64
	v_exp_f32_e32 v65, v65
	v_fma_f32 v66, v66, s63, -v100
	v_fma_f32 v67, v67, s63, -v100
	v_fma_f32 v68, v68, s63, -v100
	v_fma_f32 v69, v69, s63, -v100
	v_exp_f32_e32 v133, v70
	v_fma_f32 v70, v73, s63, -v100
	v_exp_f32_e32 v141, v141
	v_exp_f32_e32 v142, v142
	v_exp_f32_e32 v66, v66
	v_exp_f32_e32 v67, v67
	v_exp_f32_e32 v68, v68
	v_exp_f32_e32 v69, v69
	v_exp_f32_e32 v73, v70
	ds_read_b64 v[166:167], v166 offset:0x1800
	s_waitcnt lgkmcnt(0)
	v_cvt_pk_bf16_f32 v58, v58, v59
	v_cvt_pk_bf16_f32 v59, v60, v61
	v_cvt_pk_bf16_f32 v60, v62, v63
	v_cvt_pk_bf16_f32 v61, v64, v65
	v_cvt_pk_bf16_f32 v75, v141, v142
	v_cvt_pk_bf16_f32 v76, v143, v168
	v_cvt_pk_bf16_f32 v77, v169, v77
	v_cvt_pk_bf16_f32 v81, v134, v135
	v_cvt_pk_bf16_f32 v70, v66, v67
	v_cvt_pk_bf16_f32 v71, v68, v69
	v_cvt_pk_bf16_f32 v72, v127, v132
	v_cvt_pk_bf16_f32 v73, v133, v73
	s_mov_b32 s38, s36
	s_mov_b32 s39, s36
	s_mov_b32 s37, s36
	v_mov_b64_e32 v[64:65], s[38:39]
	v_mov_b64_e32 v[62:63], s[36:37]
	v_mfma_f32_16x16x32_bf16 v[54:57], v[136:139], v[74:77], v[54:57]
	s_nop 0
	v_mfma_f32_16x16x32_bf16 v[38:41], v[62:65], v[74:77], v[38:41]
	v_mfma_f32_16x16x32_bf16 v[26:29], v[62:65], v[58:61], v[26:29]
	v_mfma_f32_16x16x32_bf16 v[50:53], v[136:139], v[58:61], v[50:53]
	v_mfma_f32_16x16x32_bf16 v[46:49], v[144:147], v[74:77], v[46:49]
	v_mfma_f32_16x16x32_bf16 v[22:25], v[144:147], v[58:61], v[22:25]
	v_mfma_f32_16x16x32_bf16 v[42:45], v[148:151], v[74:77], v[42:45]
	v_mfma_f32_16x16x32_bf16 v[18:21], v[148:151], v[58:61], v[18:21]
	v_mfma_f32_16x16x32_bf16 v[34:37], v[152:155], v[74:77], v[34:37]
	v_mfma_f32_16x16x32_bf16 v[30:33], v[152:155], v[58:61], v[30:33]
	v_mfma_f32_16x16x32_bf16 v[38:41], v[62:65], v[78:81], v[38:41]
	v_mfma_f32_16x16x32_bf16 v[26:29], v[62:65], v[70:73], v[26:29]
	v_mfma_f32_16x16x32_bf16 v[66:69], v[128:131], v[78:81], v[54:57]
	v_mfma_f32_16x16x32_bf16 v[58:61], v[128:131], v[70:73], v[50:53]
	v_mfma_f32_16x16x32_bf16 v[62:65], v[156:159], v[78:81], v[46:49]
	v_mfma_f32_16x16x32_bf16 v[22:25], v[156:159], v[70:73], v[22:25]
	v_mfma_f32_16x16x32_bf16 v[42:45], v[160:163], v[78:81], v[42:45]
	v_mfma_f32_16x16x32_bf16 v[18:21], v[160:163], v[70:73], v[18:21]
	v_mfma_f32_16x16x32_bf16 v[34:37], v[164:167], v[78:81], v[34:37]
	v_mfma_f32_16x16x32_bf16 v[30:33], v[164:167], v[70:73], v[30:33]
; template <int NQ, int NKF, int MODE> ...
;     ...
;     f32x4 s[NQ][NKF];
;     const int krow = koff + l15, ksw = (krow >> 1) & 7;
;     const unsigned kad0 = kb_ + (unsigned)(krow * 128 + ((gq ^ ksw) << 4)), kad1 = kb_ + (unsigned)(krow * 128 + (((4 + gq) ^ ksw) << 4));
;     bf16x8 kfr[2][NKF];
; #pragma unroll
;     for (int ks = 0; ks < 2; ++ks)
; #pragma unroll
;         for (int kf = 0; kf < NKF; ++kf) AT_DSR128(kfr[ks][kf], (ks ? kad1 : kad0), kf * 2048);
;     float bv[NQ][NKF * 4];
;     if (MODE == 2) {
; #pragma unroll
;         for (int q = 0; q < NQ; ++q) {
;             int drq = qpos0 - q; drq = drq < 0 ? 0 : (drq > 14 ? 14 : drq);
;             const unsigned ba = nc.blane + (unsigned)(drq * 256);
; #pragma unroll
;             for (int kf = 0; kf < NKF; ++kf)
; #pragma unroll
;                 for (int r = 0; r < 4; ++r) AT_DSR32(bv[q][kf * 4 + r], ba, (kf * 16 + r) * 4);
;         }
;     }
;     const int vsw = (l15 >> 1) & 7;
;     i32x2 vlo[NKF / 2][4], vhi[NKF / 2][4];
; #pragma unroll
;     for (int q = 0; q < NQ; ++q)
; #pragma unroll
;         for (int kf = 0; kf < NKF; ++kf) s[q][kf] = (f32x4){0.f, 0.f, 0.f, 0.f};
;     if (MODE == 2) AT_LW((NQ * NKF * 4 > 15 ? 15 : NQ * NKF * 4)); else AT_LW(0);
; #pragma unroll
;     for (int ks = 0; ks < 2; ++ks)
; #pragma unroll
;         for (int kf = 0; kf < NKF; ++kf)
; #pragma unroll
;             for (int q = 0; q < NQ; ++q) s[q][kf] = mfma16(kfr[ks][kf], qf[q][ks], s[q][kf]);
;     __builtin_amdgcn_sched_barrier(0);
; #pragma unroll
;     for (int t = 0; t < NKF / 2; ++t) {
;         const int ko = koff + 32 * t + 4 * gq, ko2 = ko + 16;
;         const unsigned va = vb_ + (unsigned)(l15 * 128 + (((ko >> 3) ^ vsw) << 4) + ((ko & 4) << 1));
;         const unsigned vh = vb_ + (unsigned)(l15 * 128 + (((ko2 >> 3) ^ vsw) << 4) + ((ko2 & 4) << 1));
; #pragma unroll
; template <bool ISA>
; __device__ __forceinline__ void attn_unit(const Params& p, unsigned char* smem, int b, int hh, int blk) {
;     ...
;                 const bool skip = (t0 > qt0 + 31 + 128) || (t0 + 63 < qt0 - 128);
;                 const bool inner = (t0 >= qt0 + 31 - 128) && (t0 + 63 <= qt0 + 128);
;                 if (inner) attn_tile<NQ, 4, 0>(kb_, vb_, 0, qf, osum, o, l15, gq, 0, 0, negM2, nc);
;                 else if (!skip) attn_tile<NQ, 4, 1>(kb_, vb_, 0, qf, osum, o, l15, gq, qt0 + l15, t0, negM2, nc);
.LBB0_413:
	s_or_saveexec_b64 s[60:61], s[0:1]
	s_nop 1
	v_mov_b64_e32 v[72:73], v[64:65]
	v_mov_b64_e32 v[76:77], v[60:61]
	v_mov_b64_e32 v[80:81], v[68:69]
	v_mov_b64_e32 v[70:71], v[62:63]
	v_mov_b64_e32 v[74:75], v[58:59]
	v_mov_b64_e32 v[78:79], v[66:67]
	s_xor_b64 exec, exec, s[60:61]
	s_cbranch_execz .LBB0_404
	v_cmp_lt_i32_e64 s[0:1], v86, v105
	v_cmp_gt_i32_e64 s[6:7], v86, v106
	s_or_b64 s[0:1], s[0:1], s[6:7]
	s_and_saveexec_b64 s[6:7], s[0:1]
	s_xor_b64 s[64:65], exec, s[6:7]
	s_cbranch_execz .LBB0_418
	v_add_u32_e32 v70, 63, v86
	v_cmp_le_i32_e64 s[0:1], v86, v107
	v_cmp_ge_i32_e64 s[6:7], v70, v108
	s_and_b64 s[0:1], s[0:1], s[6:7]
	s_and_saveexec_b64 s[40:41], s[0:1]
	s_cbranch_execz .LBB0_417
	v_add_u32_e32 v160, s73, v112
	v_add_u32_e32 v70, v160, v132
	ds_read_b128 v[58:61], v70 offset:0
	ds_read_b128 v[62:65], v70 offset:0x800
	ds_read_b128 v[66:69], v70 offset:0x1000
	ds_read_b128 v[70:73], v70 offset:0x1800
	v_add_u32_e32 v131, v160, v131
	ds_read_b128 v[74:77], v131 offset:0
	ds_read_b128 v[78:81], v131 offset:0x800
	ds_read_b128 v[132:135], v131 offset:0x1000
	ds_read_b128 v[136:139], v131 offset:0x1800
	s_nop 0
	s_waitcnt lgkmcnt(7)
	v_mfma_f32_16x16x32_bf16 v[140:143], v[58:61], v[14:17], 0
	v_mfma_f32_16x16x32_bf16 v[58:61], v[58:61], v[6:9], 0
	s_waitcnt lgkmcnt(6)
	v_mfma_f32_16x16x32_bf16 v[144:147], v[62:65], v[14:17], 0
	v_mfma_f32_16x16x32_bf16 v[62:65], v[62:65], v[6:9], 0
	s_waitcnt lgkmcnt(5)
	v_mfma_f32_16x16x32_bf16 v[148:151], v[66:69], v[14:17], 0
	v_mfma_f32_16x16x32_bf16 v[66:69], v[66:69], v[6:9], 0
	s_waitcnt lgkmcnt(4)
	v_mfma_f32_16x16x32_bf16 v[152:155], v[70:73], v[14:17], 0
	v_mfma_f32_16x16x32_bf16 v[70:73], v[70:73], v[6:9], 0
	s_waitcnt lgkmcnt(3)
	v_mfma_f32_16x16x32_bf16 v[58:61], v[74:77], v[10:13], v[58:61]
	s_waitcnt lgkmcnt(2)
	v_mfma_f32_16x16x32_bf16 v[62:65], v[78:81], v[10:13], v[62:65]
	s_waitcnt lgkmcnt(1)
	v_mfma_f32_16x16x32_bf16 v[66:69], v[132:135], v[10:13], v[66:69]
	v_mfma_f32_16x16x32_bf16 v[140:143], v[74:77], v[2:5], v[140:143]
	v_mfma_f32_16x16x32_bf16 v[74:77], v[78:81], v[2:5], v[144:147]
	v_mfma_f32_16x16x32_bf16 v[78:81], v[132:135], v[2:5], v[148:151]
	s_waitcnt lgkmcnt(0)
	v_mfma_f32_16x16x32_bf16 v[132:135], v[136:139], v[2:5], v[152:155]
	v_mfma_f32_16x16x32_bf16 v[136:139], v[136:139], v[10:13], v[70:73]
	s_nop 2
	v_add_u32_e32 v70, v160, v129
	v_add_u32_e32 v71, v160, v130
	ds_read_b64 v[144:145], v70 offset:0
	ds_read_b64 v[146:147], v71 offset:0
	ds_read_b64 v[148:149], v70 offset:0x800
	ds_read_b64 v[150:151], v71 offset:0x800
	ds_read_b64 v[152:153], v70 offset:0x1000
	ds_read_b64 v[154:155], v71 offset:0x1000
	ds_read_b64 v[156:157], v70 offset:0x1800
	v_add_u32_e32 v70, v160, v127
	v_fma_f32 v127, v140, s63, -v100
	v_add_u32_e32 v140, -16, v110
	v_cmp_gt_u32_e64 s[0:1], s62, v140
	v_fma_f32 v140, v141, s63, -v100
	v_subrev_u32_e32 v141, 17, v110
	v_cmp_gt_u32_e64 s[6:7], s62, v141
	v_fma_f32 v141, v142, s63, -v100
	v_subrev_u32_e32 v142, 18, v110
	v_cmp_gt_u32_e64 s[8:9], s62, v142
	v_fma_f32 v142, v143, s63, -v100
	v_subrev_u32_e32 v143, 19, v110
	v_cmp_gt_u32_e64 s[10:11], s62, v143
	v_subrev_u32_e32 v143, 32, v110
	v_fma_f32 v74, v74, s63, -v100
	v_cmp_gt_u32_e64 s[12:13], s62, v143
	v_cndmask_b32_e64 v127, v124, v127, s[0:1]
	v_cndmask_b32_e64 v140, v124, v140, s[6:7]
	v_cndmask_b32_e64 v74, v124, v74, s[12:13]
	v_exp_f32_e32 v143, v74
	v_fma_f32 v74, v75, s63, -v100
	v_subrev_u32_e32 v75, 33, v110
	v_cmp_gt_u32_e64 s[14:15], s62, v75
	v_subrev_u32_e32 v75, 34, v110
	v_cmp_gt_u32_e64 s[16:17], s62, v75
	v_cndmask_b32_e64 v74, v124, v74, s[14:15]
	v_exp_f32_e32 v168, v74
	v_fma_f32 v74, v76, s63, -v100
	v_cndmask_b32_e64 v74, v124, v74, s[16:17]
	v_subrev_u32_e32 v75, 35, v110
	v_exp_f32_e32 v169, v74
	v_fma_f32 v74, v77, s63, -v100
	v_cmp_gt_u32_e64 s[18:19], s62, v75
	v_subrev_u32_e32 v75, 48, v110
	v_cmp_gt_u32_e64 s[20:21], s62, v75
	v_cndmask_b32_e64 v74, v124, v74, s[18:19]
	v_exp_f32_e32 v77, v74
	v_fma_f32 v74, v78, s63, -v100
	v_cndmask_b32_e64 v74, v124, v74, s[20:21]
	v_subrev_u32_e32 v75, 49, v110
	v_exp_f32_e32 v78, v74
	v_fma_f32 v74, v79, s63, -v100
	v_cmp_gt_u32_e64 s[22:23], s62, v75
	v_subrev_u32_e32 v75, 50, v110
	v_cmp_gt_u32_e64 s[24:25], s62, v75
	v_cndmask_b32_e64 v74, v124, v74, s[22:23]
	v_exp_f32_e32 v79, v74
	v_fma_f32 v74, v80, s63, -v100
	v_cndmask_b32_e64 v74, v124, v74, s[24:25]
	v_subrev_u32_e32 v75, 51, v110
	v_exp_f32_e32 v80, v74
	v_fma_f32 v74, v81, s63, -v100
	v_cmp_gt_u32_e64 s[26:27], s62, v75
	v_subrev_u32_e32 v75, 64, v110
	v_cmp_gt_u32_e64 s[28:29], s62, v75
	v_cndmask_b32_e64 v74, v124, v74, s[26:27]
	v_exp_f32_e32 v81, v74
	v_fma_f32 v74, v132, s63, -v100
	v_cndmask_b32_e64 v74, v124, v74, s[28:29]
	v_add_u32_e32 v75, 0xffffffbf, v110
	v_exp_f32_e32 v132, v74
	v_fma_f32 v74, v133, s63, -v100
	v_cmp_gt_u32_e64 s[28:29], s62, v75
	v_add_u32_e32 v75, 0xffffffbe, v110
	v_exp_f32_e32 v127, v127
	v_cndmask_b32_e64 v74, v124, v74, s[28:29]
	v_exp_f32_e32 v133, v74
; __device__ __forceinline__ f32x4 mfma16(bf16x8 a, bf16x8 b, f32x4 c) { return __builtin_amdgcn_mfma_f32_16x16x32_bf16(a, b, c, 0, 0, 0); }
; #define AT_LW(n) do { asm volatile("s_waitcnt lgkmcnt(%0)" :: "n"(n) : "memory"); __builtin_amdgcn_sched_barrier(0); } while (0)
; template <int NQ, int NKF, int MODE> ...
;     ...
;         if (MODE == 1) ub = (unsigned)((qpos0 + q * 16) - (kpos0 + gq * 4) + 128);
;         if (MODE == 2) qm = ((kpos0 >> q) & 1) ? 0xFFFFFFFFu : 0u;
; #pragma unroll
;         for (int kf = 0; kf < NKF; ++kf)
; #pragma unroll
;             for (int r = 0; r < 4; ++r) {
;                 float xv = __builtin_fmaf(s[q][kf][r], C2, MODE == 2 ? bv[q][kf * 4 + r] : negM2);
;                 if (MODE == 1) { const bool valid = (ub - (unsigned)(kf * 16 + r)) <= 256u; xv = valid ? xv : -1e30f; }
;                 s[q][kf][r] = __builtin_amdgcn_exp2f(xv);
;             }
; #pragma unroll
;         for (int t = 0; t < NKF / 2; ++t) {
;             uint4 w; w.x = pack2(s[q][2 * t][0], s[q][2 * t][1]); w.y = pack2(s[q][2 * t][2], s[q][2 * t][3]);
;             w.z = pack2(s[q][2 * t + 1][0], s[q][2 * t + 1][1]); w.w = pack2(s[q][2 * t + 1][2], s[q][2 * t + 1][3]);
;             if (MODE == 2) { w.x &= nc.cm[0] & qm; w.y &= nc.cm[1] & qm; w.z &= nc.cm[2] & qm; w.w &= nc.cm[3] & qm; }
;             pb[q][t] = __builtin_bit_cast(bf16x8, w);
;         }
;     }
;     const bf16x8 ones = {0x3F80, 0x3F80, 0x3F80, 0x3F80, 0x3F80, 0x3F80, 0x3F80, 0x3F80};
;     AT_LW(0);
; #pragma unroll
;     for (int t = 0; t < NKF / 2; ++t) {
; #pragma unroll
;         for (int q = 0; q < NQ; ++q) osum[q] = mfma16(ones, pb[q][t], osum[q]);
; #pragma unroll
;         for (int df = 0; df < 4; ++df) {
;             const bf16x8 vfr = __builtin_bit_cast(bf16x8, __builtin_shufflevector(vlo[t][df], vhi[t][df], 0, 1, 2, 3));
; #pragma unroll
;             for (int q = 0; q < NQ; ++q) o[q][df] = mfma16(vfr, pb[q][t], o[q][df]);
;         }
;     }
	v_fma_f32 v74, v134, s63, -v100
	v_cmp_gt_u32_e64 s[28:29], s62, v75
	v_add_u32_e32 v75, 0xffffffbd, v110
	v_exp_f32_e32 v140, v140
	v_cndmask_b32_e64 v74, v124, v74, s[28:29]
	v_exp_f32_e32 v134, v74
	v_fma_f32 v74, v135, s63, -v100
	v_cmp_gt_u32_e64 s[28:29], s62, v75
	v_cvt_pk_bf16_f32 v78, v78, v79
	v_cvt_pk_bf16_f32 v79, v80, v81
	v_cndmask_b32_e64 v74, v124, v74, s[28:29]
	v_exp_f32_e32 v135, v74
	v_cvt_pk_bf16_f32 v74, v127, v140
	v_cvt_pk_bf16_f32 v80, v132, v133
	v_fma_f32 v58, v58, s63, -v100
	v_cmp_gt_u32_e64 s[28:29], s62, v110
	v_add_u32_e32 v127, -1, v110
	v_fma_f32 v132, v137, s63, -v100
	v_cndmask_b32_e64 v58, v124, v58, s[28:29]
	v_fma_f32 v59, v59, s63, -v100
	v_cmp_gt_u32_e64 s[28:29], s62, v127
	v_add_u32_e32 v127, -2, v110
	v_cndmask_b32_e64 v132, v124, v132, s[22:23]
	v_cvt_pk_bf16_f32 v81, v134, v135
	v_cndmask_b32_e64 v59, v124, v59, s[28:29]
	v_fma_f32 v60, v60, s63, -v100
	v_cmp_gt_u32_e64 s[28:29], s62, v127
	v_add_u32_e32 v127, -3, v110
	v_exp_f32_e32 v134, v132
	v_fma_f32 v132, v138, s63, -v100
	v_cndmask_b32_e64 v60, v124, v60, s[28:29]
	v_fma_f32 v61, v61, s63, -v100
	v_cmp_gt_u32_e64 s[28:29], s62, v127
	v_fma_f32 v62, v62, s63, -v100
	v_fma_f32 v63, v63, s63, -v100
	v_fma_f32 v64, v64, s63, -v100
	v_fma_f32 v65, v65, s63, -v100
	v_cndmask_b32_e64 v132, v124, v132, s[24:25]
	v_cndmask_b32_e64 v61, v124, v61, s[28:29]
	v_cndmask_b32_e64 v62, v124, v62, s[0:1]
	v_cndmask_b32_e64 v63, v124, v63, s[6:7]
	v_cndmask_b32_e64 v64, v124, v64, s[8:9]
	v_cndmask_b32_e64 v65, v124, v65, s[10:11]
	v_fma_f32 v66, v66, s63, -v100
	v_fma_f32 v67, v67, s63, -v100
	v_fma_f32 v68, v68, s63, -v100
	v_fma_f32 v69, v69, s63, -v100
	v_fma_f32 v127, v136, s63, -v100
	v_exp_f32_e32 v135, v132
	v_fma_f32 v132, v139, s63, -v100
	v_cndmask_b32_e64 v141, v124, v141, s[8:9]
	v_cndmask_b32_e64 v142, v124, v142, s[10:11]
	v_exp_f32_e32 v58, v58
	v_exp_f32_e32 v59, v59
	v_exp_f32_e32 v60, v60
	v_exp_f32_e32 v61, v61
	v_exp_f32_e32 v62, v62
	v_exp_f32_e32 v63, v63
	v_exp_f32_e32 v64, v64
	v_exp_f32_e32 v65, v65
	v_cndmask_b32_e64 v66, v124, v66, s[12:13]
	v_cndmask_b32_e64 v67, v124, v67, s[14:15]
	v_cndmask_b32_e64 v68, v124, v68, s[16:17]
	v_cndmask_b32_e64 v69, v124, v69, s[18:19]
	v_cndmask_b32_e64 v127, v124, v127, s[20:21]
	v_cndmask_b32_e64 v132, v124, v132, s[26:27]
	v_add_u32_e32 v72, v160, v128
	v_exp_f32_e32 v141, v141
	v_exp_f32_e32 v142, v142
	v_exp_f32_e32 v66, v66
	v_exp_f32_e32 v67, v67
	v_exp_f32_e32 v68, v68
	v_exp_f32_e32 v69, v69
	v_exp_f32_e32 v127, v127
	v_exp_f32_e32 v136, v132
	ds_read_b64 v[158:159], v71 offset:0x1800
	ds_read_b64 v[128:129], v70 offset:0
	ds_read_b64 v[130:131], v72 offset:0
	ds_read_b64 v[160:161], v70 offset:0x800
	ds_read_b64 v[162:163], v72 offset:0x800
	ds_read_b64 v[164:165], v70 offset:0x1000
	ds_read_b64 v[166:167], v72 offset:0x1000
	ds_read_b64 v[70:71], v70 offset:0x1800
	ds_read_b64 v[72:73], v72 offset:0x1800
	s_waitcnt lgkmcnt(0)
	v_cvt_pk_bf16_f32 v58, v58, v59
	v_cvt_pk_bf16_f32 v59, v60, v61
	v_cvt_pk_bf16_f32 v60, v62, v63
	v_cvt_pk_bf16_f32 v61, v64, v65
	v_cvt_pk_bf16_f32 v75, v141, v142
	v_cvt_pk_bf16_f32 v76, v143, v168
	v_cvt_pk_bf16_f32 v77, v169, v77
	v_cvt_pk_bf16_f32 v132, v66, v67
	v_cvt_pk_bf16_f32 v133, v68, v69
	v_cvt_pk_bf16_f32 v134, v127, v134
	v_cvt_pk_bf16_f32 v135, v135, v136
	s_mov_b32 s38, s36
	s_mov_b32 s39, s36
	s_mov_b32 s37, s36
	v_mov_b64_e32 v[64:65], s[38:39]
	v_mov_b64_e32 v[62:63], s[36:37]
	v_mfma_f32_16x16x32_bf16 v[54:57], v[144:147], v[74:77], v[54:57]
	v_mfma_f32_16x16x32_bf16 v[50:53], v[144:147], v[58:61], v[50:53]
	v_mfma_f32_16x16x32_bf16 v[46:49], v[148:151], v[74:77], v[46:49]
	v_mfma_f32_16x16x32_bf16 v[38:41], v[62:65], v[74:77], v[38:41]
	v_mfma_f32_16x16x32_bf16 v[26:29], v[62:65], v[58:61], v[26:29]
	v_mfma_f32_16x16x32_bf16 v[22:25], v[148:151], v[58:61], v[22:25]
	v_mfma_f32_16x16x32_bf16 v[42:45], v[152:155], v[74:77], v[42:45]
	v_mfma_f32_16x16x32_bf16 v[18:21], v[152:155], v[58:61], v[18:21]
	v_mfma_f32_16x16x32_bf16 v[34:37], v[156:159], v[74:77], v[34:37]
	v_mfma_f32_16x16x32_bf16 v[30:33], v[156:159], v[58:61], v[30:33]
	v_mfma_f32_16x16x32_bf16 v[54:57], v[128:131], v[78:81], v[54:57]
	v_mfma_f32_16x16x32_bf16 v[50:53], v[128:131], v[132:135], v[50:53]
	v_mfma_f32_16x16x32_bf16 v[46:49], v[160:163], v[78:81], v[46:49]
	s_nop 5
	v_mov_b64_e32 v[68:69], v[56:57]
	v_mov_b64_e32 v[60:61], v[52:53]
	v_mov_b64_e32 v[66:67], v[54:55]
	v_mfma_f32_16x16x32_bf16 v[38:41], v[62:65], v[78:81], v[38:41]
	v_mov_b64_e32 v[58:59], v[50:51]
	v_mfma_f32_16x16x32_bf16 v[26:29], v[62:65], v[132:135], v[26:29]
	v_mov_b64_e32 v[64:65], v[48:49]
	v_mov_b64_e32 v[62:63], v[46:47]
	v_mfma_f32_16x16x32_bf16 v[22:25], v[160:163], v[132:135], v[22:25]
	v_mfma_f32_16x16x32_bf16 v[42:45], v[164:167], v[78:81], v[42:45]
	v_mfma_f32_16x16x32_bf16 v[18:21], v[164:167], v[132:135], v[18:21]
	v_mfma_f32_16x16x32_bf16 v[34:37], v[70:73], v[78:81], v[34:37]
	v_mfma_f32_16x16x32_bf16 v[30:33], v[70:73], v[132:135], v[30:33]

; template <int NQ, int NKF, int MODE> ...
;     ...
;     f32x4 s[NQ][NKF];
;     const int krow = koff + l15, ksw = (krow >> 1) & 7;
;     const unsigned kad0 = kb_ + (unsigned)(krow * 128 + ((gq ^ ksw) << 4)), kad1 = kb_ + (unsigned)(krow * 128 + (((4 + gq) ^ ksw) << 4));
;     bf16x8 kfr[2][NKF];
; #pragma unroll
;     for (int ks = 0; ks < 2; ++ks)
; #pragma unroll
;         for (int kf = 0; kf < NKF; ++kf) AT_DSR128(kfr[ks][kf], (ks ? kad1 : kad0), kf * 2048);
;     float bv[NQ][NKF * 4];
;     if (MODE == 2) {
; #pragma unroll
;         for (int q = 0; q < NQ; ++q) {
;             int drq = qpos0 - q; drq = drq < 0 ? 0 : (drq > 14 ? 14 : drq);
;             const unsigned ba = nc.blane + (unsigned)(drq * 256);
; #pragma unroll
;             for (int kf = 0; kf < NKF; ++kf)
; #pragma unroll
;                 for (int r = 0; r < 4; ++r) AT_DSR32(bv[q][kf * 4 + r], ba, (kf * 16 + r) * 4);
;         }
;     }
;     const int vsw = (l15 >> 1) & 7;
;     i32x2 vlo[NKF / 2][4], vhi[NKF / 2][4];
; #pragma unroll
;     for (int q = 0; q < NQ; ++q)
; #pragma unroll
;         for (int kf = 0; kf < NKF; ++kf) s[q][kf] = (f32x4){0.f, 0.f, 0.f, 0.f};
;     if (MODE == 2) AT_LW((NQ * NKF * 4 > 15 ? 15 : NQ * NKF * 4)); else AT_LW(0);
; #pragma unroll
;     for (int ks = 0; ks < 2; ++ks)
; #pragma unroll
;         for (int kf = 0; kf < NKF; ++kf)
; #pragma unroll
;             for (int q = 0; q < NQ; ++q) s[q][kf] = mfma16(kfr[ks][kf], qf[q][ks], s[q][kf]);
;     __builtin_amdgcn_sched_barrier(0);
; #pragma unroll
;     for (int t = 0; t < NKF / 2; ++t) {
;         const int ko = koff + 32 * t + 4 * gq, ko2 = ko + 16;
;         const unsigned va = vb_ + (unsigned)(l15 * 128 + (((ko >> 3) ^ vsw) << 4) + ((ko & 4) << 1));
;         const unsigned vh = vb_ + (unsigned)(l15 * 128 + (((ko2 >> 3) ^ vsw) << 4) + ((ko2 & 4) << 1));
; #pragma unroll
;         for (int df = 0; df < 4; ++df) { AT_DSR64(vlo[t][df], va, df * 2048); AT_DSR64(vhi[t][df], vh, df * 2048); }
;     }
;     if (MODE == 2) AT_LW(NKF * 4);
;     bf16x8 pb[NQ][NKF / 2];
; #pragma unroll
;     for (int q = 0; q < NQ; ++q) {
;         unsigned ub = 0; unsigned qm = 0xFFFFFFFFu;
;         if (MODE == 1) ub = (unsigned)((qpos0 + q * 16) - (kpos0 + gq * 4) + 128);
;         if (MODE == 2) qm = ((kpos0 >> q) & 1) ? 0xFFFFFFFFu : 0u;
; #pragma unroll
;         for (int kf = 0; kf < NKF; ++kf)
; #pragma unroll
.LBB0_418:
	s_andn2_saveexec_b64 s[0:1], s[64:65]
	s_cbranch_execz .LBB0_403
	v_add_u32_e32 v156, s73, v112
	v_add_u32_e32 v70, v156, v132
	ds_read_b128 v[58:61], v70 offset:0
	ds_read_b128 v[62:65], v70 offset:0x800
	ds_read_b128 v[66:69], v70 offset:0x1000
	ds_read_b128 v[70:73], v70 offset:0x1800
	v_add_u32_e32 v131, v156, v131
	ds_read_b128 v[74:77], v131 offset:0
	ds_read_b128 v[78:81], v131 offset:0x800
	ds_read_b128 v[132:135], v131 offset:0x1000
	ds_read_b128 v[136:139], v131 offset:0x1800
	s_nop 0
	s_waitcnt lgkmcnt(7)
	v_mfma_f32_16x16x32_bf16 v[140:143], v[58:61], v[14:17], 0
	v_mfma_f32_16x16x32_bf16 v[58:61], v[58:61], v[6:9], 0
	s_waitcnt lgkmcnt(6)
	v_mfma_f32_16x16x32_bf16 v[144:147], v[62:65], v[14:17], 0
	v_mfma_f32_16x16x32_bf16 v[62:65], v[62:65], v[6:9], 0
	s_waitcnt lgkmcnt(5)
	v_mfma_f32_16x16x32_bf16 v[148:151], v[66:69], v[14:17], 0
	v_mfma_f32_16x16x32_bf16 v[66:69], v[66:69], v[6:9], 0
	s_waitcnt lgkmcnt(4)
	v_mfma_f32_16x16x32_bf16 v[152:155], v[70:73], v[14:17], 0
	v_mfma_f32_16x16x32_bf16 v[70:73], v[70:73], v[6:9], 0
	s_waitcnt lgkmcnt(3)
	v_mfma_f32_16x16x32_bf16 v[58:61], v[74:77], v[10:13], v[58:61]
	s_waitcnt lgkmcnt(2)
	v_mfma_f32_16x16x32_bf16 v[62:65], v[78:81], v[10:13], v[62:65]
	s_waitcnt lgkmcnt(1)
	v_mfma_f32_16x16x32_bf16 v[66:69], v[132:135], v[10:13], v[66:69]
	v_mfma_f32_16x16x32_bf16 v[140:143], v[74:77], v[2:5], v[140:143]
	v_mfma_f32_16x16x32_bf16 v[74:77], v[78:81], v[2:5], v[144:147]
	v_mfma_f32_16x16x32_bf16 v[78:81], v[132:135], v[2:5], v[148:151]
	s_waitcnt lgkmcnt(0)
	v_mfma_f32_16x16x32_bf16 v[132:135], v[136:139], v[2:5], v[152:155]
	v_mfma_f32_16x16x32_bf16 v[70:73], v[136:139], v[10:13], v[70:73]
	v_add_u32_e32 v129, v156, v129
	v_add_u32_e32 v130, v156, v130
	v_add_u32_e32 v127, v156, v127
	s_nop 1
	v_fma_f32 v74, v74, s63, -v100
	ds_read_b64 v[136:137], v129 offset:0
	ds_read_b64 v[138:139], v130 offset:0
	ds_read_b64 v[144:145], v129 offset:0x800
	ds_read_b64 v[146:147], v130 offset:0x800
	ds_read_b64 v[148:149], v129 offset:0x1000
	ds_read_b64 v[150:151], v130 offset:0x1000
	ds_read_b64 v[152:153], v129 offset:0x1800
	ds_read_b64 v[154:155], v130 offset:0x1800
	v_add_u32_e32 v166, v156, v128
	ds_read_b64 v[128:129], v127 offset:0
	ds_read_b64 v[130:131], v166 offset:0
	ds_read_b64 v[156:157], v127 offset:0x800
	ds_read_b64 v[158:159], v166 offset:0x800
	ds_read_b64 v[160:161], v127 offset:0x1000
	ds_read_b64 v[162:163], v166 offset:0x1000
	ds_read_b64 v[164:165], v127 offset:0x1800
	v_fma_f32 v127, v140, s63, -v100
	v_fma_f32 v140, v141, s63, -v100
	v_fma_f32 v141, v142, s63, -v100
	v_fma_f32 v142, v143, s63, -v100
	v_exp_f32_e32 v143, v74
	v_fma_f32 v74, v75, s63, -v100
	v_exp_f32_e32 v168, v74
	v_fma_f32 v74, v76, s63, -v100
	v_exp_f32_e32 v169, v74
	v_fma_f32 v74, v77, s63, -v100
	v_exp_f32_e32 v77, v74
	v_fma_f32 v74, v78, s63, -v100
	v_exp_f32_e32 v78, v74
	v_fma_f32 v74, v79, s63, -v100
	v_exp_f32_e32 v79, v74
	v_fma_f32 v74, v80, s63, -v100
	v_exp_f32_e32 v80, v74
	v_fma_f32 v74, v81, s63, -v100
	v_exp_f32_e32 v81, v74
	v_fma_f32 v74, v132, s63, -v100
	v_exp_f32_e32 v127, v127
	v_exp_f32_e32 v140, v140
	v_exp_f32_e32 v132, v74
	v_fma_f32 v74, v133, s63, -v100
	v_exp_f32_e32 v133, v74
	v_fma_f32 v74, v134, s63, -v100
	v_exp_f32_e32 v134, v74
	v_fma_f32 v74, v135, s63, -v100
	v_fma_f32 v70, v70, s63, -v100
	v_exp_f32_e32 v135, v74
	v_cvt_pk_bf16_f32 v74, v127, v140
	v_exp_f32_e32 v127, v70
	v_fma_f32 v70, v71, s63, -v100
	v_cvt_pk_bf16_f32 v78, v78, v79
	v_cvt_pk_bf16_f32 v79, v80, v81
	v_cvt_pk_bf16_f32 v80, v132, v133
	v_fma_f32 v58, v58, s63, -v100
	v_fma_f32 v59, v59, s63, -v100
	v_fma_f32 v60, v60, s63, -v100
	v_fma_f32 v61, v61, s63, -v100
	v_fma_f32 v62, v62, s63, -v100
	v_fma_f32 v63, v63, s63, -v100
	v_fma_f32 v64, v64, s63, -v100
	v_fma_f32 v65, v65, s63, -v100
	v_exp_f32_e32 v132, v70
	v_fma_f32 v70, v72, s63, -v100
	v_exp_f32_e32 v58, v58
	v_exp_f32_e32 v59, v59
	v_exp_f32_e32 v60, v60
	v_exp_f32_e32 v61, v61
	v_exp_f32_e32 v62, v62
	v_exp_f32_e32 v63, v63
	v_exp_f32_e32 v64, v64
	v_exp_f32_e32 v65, v65
	v_fma_f32 v66, v66, s63, -v100
	v_fma_f32 v67, v67, s63, -v100
	v_fma_f32 v68, v68, s63, -v100
	v_fma_f32 v69, v69, s63, -v100
	v_exp_f32_e32 v133, v70
	v_fma_f32 v70, v73, s63, -v100
	v_exp_f32_e32 v141, v141
	v_exp_f32_e32 v142, v142
	v_exp_f32_e32 v66, v66
	v_exp_f32_e32 v67, v67
	v_exp_f32_e32 v68, v68
	v_exp_f32_e32 v69, v69
	v_exp_f32_e32 v73, v70
	ds_read_b64 v[166:167], v166 offset:0x1800
	s_waitcnt lgkmcnt(0)
	v_cvt_pk_bf16_f32 v58, v58, v59
	v_cvt_pk_bf16_f32 v59, v60, v61
	v_cvt_pk_bf16_f32 v60, v62, v63
	v_cvt_pk_bf16_f32 v61, v64, v65
	v_cvt_pk_bf16_f32 v75, v141, v142
	v_cvt_pk_bf16_f32 v76, v143, v168
	v_cvt_pk_bf16_f32 v77, v169, v77
	v_cvt_pk_bf16_f32 v81, v134, v135
	v_cvt_pk_bf16_f32 v70, v66, v67
	v_cvt_pk_bf16_f32 v71, v68, v69
	v_cvt_pk_bf16_f32 v72, v127, v132
	v_cvt_pk_bf16_f32 v73, v133, v73
	s_mov_b32 s38, s36
	s_mov_b32 s39, s36
	s_mov_b32 s37, s36
	v_mov_b64_e32 v[64:65], s[38:39]
	v_mov_b64_e32 v[62:63], s[36:37]
	v_mfma_f32_16x16x32_bf16 v[54:57], v[136:139], v[74:77], v[54:57]
	v_mfma_f32_16x16x32_bf16 v[50:53], v[136:139], v[58:61], v[50:53]
	v_mfma_f32_16x16x32_bf16 v[46:49], v[144:147], v[74:77], v[46:49]
	v_mfma_f32_16x16x32_bf16 v[38:41], v[62:65], v[74:77], v[38:41]
	v_mfma_f32_16x16x32_bf16 v[26:29], v[62:65], v[58:61], v[26:29]
	v_mfma_f32_16x16x32_bf16 v[22:25], v[144:147], v[58:61], v[22:25]
	v_mfma_f32_16x16x32_bf16 v[42:45], v[148:151], v[74:77], v[42:45]
	v_mfma_f32_16x16x32_bf16 v[18:21], v[148:151], v[58:61], v[18:21]
	v_mfma_f32_16x16x32_bf16 v[34:37], v[152:155], v[74:77], v[34:37]
	v_mfma_f32_16x16x32_bf16 v[30:33], v[152:155], v[58:61], v[30:33]
	v_mfma_f32_16x16x32_bf16 v[54:57], v[128:131], v[78:81], v[54:57]
	v_mfma_f32_16x16x32_bf16 v[50:53], v[128:131], v[70:73], v[50:53]
	v_mfma_f32_16x16x32_bf16 v[46:49], v[156:159], v[78:81], v[46:49]
	s_nop 5
	v_mov_b64_e32 v[68:69], v[56:57]
	v_mov_b64_e32 v[60:61], v[52:53]
	v_mov_b64_e32 v[66:67], v[54:55]
	v_mfma_f32_16x16x32_bf16 v[38:41], v[62:65], v[78:81], v[38:41]
	v_mov_b64_e32 v[58:59], v[50:51]
	v_mfma_f32_16x16x32_bf16 v[26:29], v[62:65], v[70:73], v[26:29]
	v_mov_b64_e32 v[64:65], v[48:49]
	v_mov_b64_e32 v[62:63], v[46:47]
	v_mfma_f32_16x16x32_bf16 v[22:25], v[156:159], v[70:73], v[22:25]
	v_mfma_f32_16x16x32_bf16 v[42:45], v[160:163], v[78:81], v[42:45]
	v_mfma_f32_16x16x32_bf16 v[18:21], v[160:163], v[70:73], v[18:21]
	v_mfma_f32_16x16x32_bf16 v[34:37], v[164:167], v[78:81], v[34:37]
	v_mfma_f32_16x16x32_bf16 v[30:33], v[164:167], v[70:73], v[30:33]
	s_branch .LBB0_403
